# fp8 GEMM K-loops: trailing wave half issues the stages of phases 2-4 one barrier earlier (own code path), leading half waits one barrier later: every staged piece gets one more barrier interval in fli
# baseline (speedup 1.0000x reference)
.Lrw_done_ip8_0:
	s_waitcnt lgkmcnt(0)
	s_barrier
	s_setprio 1
	s_waitcnt lgkmcnt(0)
	v_mfma_scale_f32_16x16x128_f8f6f4 v[158:161], v[18:25], v[172:179], 0, v234, v235 op_sel_hi:[0,0,0]
	v_mfma_scale_f32_16x16x128_f8f6f4 v[154:157], v[26:33], v[172:179], 0, v234, v235 op_sel_hi:[0,0,0]
	v_mfma_scale_f32_16x16x128_f8f6f4 v[150:153], v[18:25], v[198:205], 0, v234, v235 op_sel_hi:[0,0,0]
	v_mfma_scale_f32_16x16x128_f8f6f4 v[146:149], v[26:33], v[198:205], 0, v234, v235 op_sel_hi:[0,0,0]
	v_mfma_scale_f32_16x16x128_f8f6f4 v[142:145], v[18:25], v[206:213], 0, v234, v235 op_sel_hi:[0,0,0]
	v_mfma_scale_f32_16x16x128_f8f6f4 v[138:141], v[26:33], v[206:213], 0, v234, v235 op_sel_hi:[0,0,0]
	v_mfma_scale_f32_16x16x128_f8f6f4 v[134:137], v[18:25], v[216:223], 0, v234, v235 op_sel_hi:[0,0,0]
	v_mfma_scale_f32_16x16x128_f8f6f4 v[130:133], v[26:33], v[216:223], 0, v234, v235 op_sel_hi:[0,0,0]
	s_setprio 0
	s_setprio 1
	v_mfma_scale_f32_16x16x128_f8f6f4 v[126:129], v[2:9], v[172:179], 0, v234, v235 op_sel_hi:[0,0,0]
	v_mfma_scale_f32_16x16x128_f8f6f4 v[122:125], v[10:17], v[172:179], 0, v234, v235 op_sel_hi:[0,0,0]
	v_mfma_scale_f32_16x16x128_f8f6f4 v[118:121], v[2:9], v[198:205], 0, v234, v235 op_sel_hi:[0,0,0]
	v_mfma_scale_f32_16x16x128_f8f6f4 v[114:117], v[10:17], v[198:205], 0, v234, v235 op_sel_hi:[0,0,0]
	v_mfma_scale_f32_16x16x128_f8f6f4 v[110:113], v[2:9], v[206:213], 0, v234, v235 op_sel_hi:[0,0,0]
	v_mfma_scale_f32_16x16x128_f8f6f4 v[106:109], v[10:17], v[206:213], 0, v234, v235 op_sel_hi:[0,0,0]
	v_mfma_scale_f32_16x16x128_f8f6f4 v[102:105], v[2:9], v[216:223], 0, v234, v235 op_sel_hi:[0,0,0]
	v_mfma_scale_f32_16x16x128_f8f6f4 v[98:101], v[10:17], v[216:223], 0, v234, v235 op_sel_hi:[0,0,0]
	s_setprio 0
	s_nop 7
	v_lshl_add_u64 v[172:173], s[44:45], 0, v[0:1]
	s_mov_b64 s[74:75], 0x100
	s_mov_b32 m0, s58
	v_lshl_add_u64 v[174:175], v[172:173], 0, s[74:75]
	global_load_lds_dwordx4 v[174:175], off
	v_lshl_add_u64 v[174:175], s[44:45], 0, v[166:167]
	s_add_u32 s48, s44, 0x20100
	v_lshl_add_u64 v[176:177], v[174:175], 0, s[74:75]
	s_mov_b32 m0, s59
	s_addc_u32 s49, s45, 0
	global_load_lds_dwordx4 v[176:177], off
	v_lshl_add_u64 v[176:177], s[48:49], 0, v[0:1]
	s_mov_b32 m0, s60
	s_nop 0
	global_load_lds_dwordx4 v[176:177], off
	v_lshl_add_u64 v[176:177], s[48:49], 0, v[166:167]
	s_mov_b32 m0, s61
	s_nop 0
	global_load_lds_dwordx4 v[176:177], off
	v_lshl_add_u64 v[176:177], s[46:47], 0, v[162:163]
	v_lshl_add_u64 v[178:179], v[176:177], 0, s[74:75]
	s_mov_b32 m0, s57
	s_nop 0
	global_load_lds_dwordx4 v[178:179], off
	v_lshl_add_u64 v[178:179], s[46:47], 0, v[164:165]
	v_lshl_add_u64 v[232:233], v[178:179], 0, s[74:75]
	s_mov_b32 m0, s62
	s_nop 0
	global_load_lds_dwordx4 v[232:233], off
	s_barrier
	ds_read_b128 v[198:201], v196 offset:16384
	ds_read_b128 v[202:205], v196 offset:17408
	ds_read_b128 v[206:209], v196 offset:18432
	ds_read_b128 v[210:213], v196 offset:19456
	ds_read_b128 v[216:219], v196 offset:20480
	ds_read_b128 v[220:223], v196 offset:21504
	ds_read_b128 v[224:227], v196 offset:22528
	ds_read_b128 v[228:231], v196 offset:23552
	s_cmp_eq_u32 s50, 1
	s_cbranch_scc1 .Lrw_first_ip8_1
	s_waitcnt vmcnt(24)
	s_branch .Lrw_done_ip8_1

.Lrw_done_ip8_1:
	s_waitcnt lgkmcnt(0)
	s_barrier
	s_setprio 1
	s_waitcnt lgkmcnt(0)
	v_mfma_scale_f32_16x16x128_f8f6f4 v[94:97], v[18:25], v[198:205], 0, v234, v235 op_sel_hi:[0,0,0]
	v_mfma_scale_f32_16x16x128_f8f6f4 v[90:93], v[26:33], v[198:205], 0, v234, v235 op_sel_hi:[0,0,0]
	v_mfma_scale_f32_16x16x128_f8f6f4 v[86:89], v[18:25], v[206:213], 0, v234, v235 op_sel_hi:[0,0,0]
	v_mfma_scale_f32_16x16x128_f8f6f4 v[82:85], v[26:33], v[206:213], 0, v234, v235 op_sel_hi:[0,0,0]
	v_mfma_scale_f32_16x16x128_f8f6f4 v[78:81], v[18:25], v[216:223], 0, v234, v235 op_sel_hi:[0,0,0]
	v_mfma_scale_f32_16x16x128_f8f6f4 v[74:77], v[26:33], v[216:223], 0, v234, v235 op_sel_hi:[0,0,0]
	v_mfma_scale_f32_16x16x128_f8f6f4 v[70:73], v[18:25], v[224:231], 0, v234, v235 op_sel_hi:[0,0,0]
	v_mfma_scale_f32_16x16x128_f8f6f4 v[66:69], v[26:33], v[224:231], 0, v234, v235 op_sel_hi:[0,0,0]
	s_setprio 0
	s_setprio 1
	v_mfma_scale_f32_16x16x128_f8f6f4 v[62:65], v[2:9], v[198:205], 0, v234, v235 op_sel_hi:[0,0,0]
	v_mfma_scale_f32_16x16x128_f8f6f4 v[58:61], v[10:17], v[198:205], 0, v234, v235 op_sel_hi:[0,0,0]
	v_mfma_scale_f32_16x16x128_f8f6f4 v[54:57], v[2:9], v[206:213], 0, v234, v235 op_sel_hi:[0,0,0]
	v_mfma_scale_f32_16x16x128_f8f6f4 v[50:53], v[10:17], v[206:213], 0, v234, v235 op_sel_hi:[0,0,0]
	v_mfma_scale_f32_16x16x128_f8f6f4 v[46:49], v[2:9], v[216:223], 0, v234, v235 op_sel_hi:[0,0,0]
	v_mfma_scale_f32_16x16x128_f8f6f4 v[42:45], v[10:17], v[216:223], 0, v234, v235 op_sel_hi:[0,0,0]
	v_mfma_scale_f32_16x16x128_f8f6f4 v[38:41], v[2:9], v[224:231], 0, v234, v235 op_sel_hi:[0,0,0]
	v_mfma_scale_f32_16x16x128_f8f6f4 v[34:37], v[10:17], v[224:231], 0, v234, v235 op_sel_hi:[0,0,0]
	s_setprio 0
	s_nop 7
	s_add_u32 s48, s46, 0x20100
	s_addc_u32 s49, s47, 0
	s_mov_b32 m0, s63
	v_lshl_add_u64 v[232:233], s[48:49], 0, v[162:163]
	global_load_lds_dwordx4 v[232:233], off
	v_lshl_add_u64 v[232:233], s[48:49], 0, v[164:165]
	s_mov_b32 m0, s64
	s_nop 0
	global_load_lds_dwordx4 v[232:233], off
	s_barrier
	ds_read_b128 v[18:21], v188
	ds_read_b128 v[22:25], v189
	ds_read_b128 v[26:29], v190
	ds_read_b128 v[30:33], v191
	ds_read_b128 v[2:5], v192
	ds_read_b128 v[6:9], v193
	ds_read_b128 v[10:13], v194
	ds_read_b128 v[14:17], v195
	ds_read_b128 v[198:201], v196 offset:32768
	ds_read_b128 v[202:205], v196 offset:33792
	ds_read_b128 v[206:209], v196 offset:34816
	ds_read_b128 v[210:213], v196 offset:35840
	ds_read_b128 v[216:219], v196 offset:36864
	ds_read_b128 v[220:223], v196 offset:37888
	ds_read_b128 v[224:227], v196 offset:38912
	ds_read_b128 v[228:231], v196 offset:39936
	s_waitcnt vmcnt(8)
	s_waitcnt lgkmcnt(0)
	s_barrier
	s_setprio 1
	s_waitcnt lgkmcnt(0)
	v_mfma_scale_f32_16x16x128_f8f6f4 v[158:161], v[18:25], v[198:205], v[158:161], v234, v235 op_sel_hi:[0,0,0]
	v_mfma_scale_f32_16x16x128_f8f6f4 v[154:157], v[26:33], v[198:205], v[154:157], v234, v235 op_sel_hi:[0,0,0]
	v_mfma_scale_f32_16x16x128_f8f6f4 v[150:153], v[18:25], v[206:213], v[150:153], v234, v235 op_sel_hi:[0,0,0]
	v_mfma_scale_f32_16x16x128_f8f6f4 v[146:149], v[26:33], v[206:213], v[146:149], v234, v235 op_sel_hi:[0,0,0]
	v_mfma_scale_f32_16x16x128_f8f6f4 v[142:145], v[18:25], v[216:223], v[142:145], v234, v235 op_sel_hi:[0,0,0]
	v_mfma_scale_f32_16x16x128_f8f6f4 v[138:141], v[26:33], v[216:223], v[138:141], v234, v235 op_sel_hi:[0,0,0]
	v_mfma_scale_f32_16x16x128_f8f6f4 v[134:137], v[18:25], v[224:231], v[134:137], v234, v235 op_sel_hi:[0,0,0]
	v_mfma_scale_f32_16x16x128_f8f6f4 v[130:133], v[26:33], v[224:231], v[130:133], v234, v235 op_sel_hi:[0,0,0]
	s_setprio 0
	s_setprio 1
	v_mfma_scale_f32_16x16x128_f8f6f4 v[126:129], v[2:9], v[198:205], v[126:129], v234, v235 op_sel_hi:[0,0,0]
	v_mfma_scale_f32_16x16x128_f8f6f4 v[122:125], v[10:17], v[198:205], v[122:125], v234, v235 op_sel_hi:[0,0,0]
	v_mfma_scale_f32_16x16x128_f8f6f4 v[118:121], v[2:9], v[206:213], v[118:121], v234, v235 op_sel_hi:[0,0,0]
	v_mfma_scale_f32_16x16x128_f8f6f4 v[114:117], v[10:17], v[206:213], v[114:117], v234, v235 op_sel_hi:[0,0,0]
	v_mfma_scale_f32_16x16x128_f8f6f4 v[110:113], v[2:9], v[216:223], v[110:113], v234, v235 op_sel_hi:[0,0,0]
	v_mfma_scale_f32_16x16x128_f8f6f4 v[106:109], v[10:17], v[216:223], v[106:109], v234, v235 op_sel_hi:[0,0,0]
	v_mfma_scale_f32_16x16x128_f8f6f4 v[102:105], v[2:9], v[224:231], v[102:105], v234, v235 op_sel_hi:[0,0,0]
	v_mfma_scale_f32_16x16x128_f8f6f4 v[98:101], v[10:17], v[224:231], v[98:101], v234, v235 op_sel_hi:[0,0,0]
	s_setprio 0
	s_nop 7
	s_mov_b64 s[74:75], 0x180
	s_mov_b32 m0, s7
	v_lshl_add_u64 v[172:173], v[172:173], 0, s[74:75]
	s_add_u32 s48, s44, 0x20180
	global_load_lds_dwordx4 v[172:173], off
	v_lshl_add_u64 v[172:173], v[174:175], 0, s[74:75]
	s_mov_b32 m0, s65
	s_addc_u32 s49, s45, 0
	global_load_lds_dwordx4 v[172:173], off
	v_lshl_add_u64 v[172:173], s[48:49], 0, v[0:1]
	s_mov_b32 m0, s13
	s_nop 0
	global_load_lds_dwordx4 v[172:173], off
	v_lshl_add_u64 v[172:173], s[48:49], 0, v[166:167]
	s_mov_b32 m0, s51
	s_nop 0
	global_load_lds_dwordx4 v[172:173], off
	v_lshl_add_u64 v[172:173], v[176:177], 0, s[74:75]
	s_mov_b32 m0, s68
	s_nop 0
	global_load_lds_dwordx4 v[172:173], off
	v_lshl_add_u64 v[172:173], v[178:179], 0, s[74:75]
	s_mov_b32 m0, s52
	s_nop 0
	global_load_lds_dwordx4 v[172:173], off
	s_barrier
	ds_read_b128 v[198:201], v196 offset:49152
	ds_read_b128 v[202:205], v196 offset:50176
	ds_read_b128 v[206:209], v196 offset:51200
	ds_read_b128 v[210:213], v196 offset:52224
	ds_read_b128 v[216:219], v196 offset:53248
	ds_read_b128 v[220:223], v196 offset:54272
	ds_read_b128 v[224:227], v196 offset:55296
	ds_read_b128 v[228:231], v196 offset:56320
	s_waitcnt vmcnt(8)
	s_waitcnt lgkmcnt(0)
	s_barrier
	s_setprio 1
	s_waitcnt lgkmcnt(0)
	v_mfma_scale_f32_16x16x128_f8f6f4 v[94:97], v[18:25], v[198:205], v[94:97], v234, v235 op_sel_hi:[0,0,0]
	v_mfma_scale_f32_16x16x128_f8f6f4 v[90:93], v[26:33], v[198:205], v[90:93], v234, v235 op_sel_hi:[0,0,0]
	v_mfma_scale_f32_16x16x128_f8f6f4 v[86:89], v[18:25], v[206:213], v[86:89], v234, v235 op_sel_hi:[0,0,0]
	v_mfma_scale_f32_16x16x128_f8f6f4 v[82:85], v[26:33], v[206:213], v[82:85], v234, v235 op_sel_hi:[0,0,0]
	v_mfma_scale_f32_16x16x128_f8f6f4 v[78:81], v[18:25], v[216:223], v[78:81], v234, v235 op_sel_hi:[0,0,0]
	v_mfma_scale_f32_16x16x128_f8f6f4 v[74:77], v[26:33], v[216:223], v[74:77], v234, v235 op_sel_hi:[0,0,0]
	v_mfma_scale_f32_16x16x128_f8f6f4 v[70:73], v[18:25], v[224:231], v[70:73], v234, v235 op_sel_hi:[0,0,0]
	v_mfma_scale_f32_16x16x128_f8f6f4 v[66:69], v[26:33], v[224:231], v[66:69], v234, v235 op_sel_hi:[0,0,0]
	s_setprio 0
	s_setprio 1
	v_mfma_scale_f32_16x16x128_f8f6f4 v[62:65], v[2:9], v[198:205], v[62:65], v234, v235 op_sel_hi:[0,0,0]
	v_mfma_scale_f32_16x16x128_f8f6f4 v[58:61], v[10:17], v[198:205], v[58:61], v234, v235 op_sel_hi:[0,0,0]
	v_mfma_scale_f32_16x16x128_f8f6f4 v[54:57], v[2:9], v[206:213], v[54:57], v234, v235 op_sel_hi:[0,0,0]
	v_mfma_scale_f32_16x16x128_f8f6f4 v[50:53], v[10:17], v[206:213], v[50:53], v234, v235 op_sel_hi:[0,0,0]
	v_mfma_scale_f32_16x16x128_f8f6f4 v[46:49], v[2:9], v[216:223], v[46:49], v234, v235 op_sel_hi:[0,0,0]
	v_mfma_scale_f32_16x16x128_f8f6f4 v[42:45], v[10:17], v[216:223], v[42:45], v234, v235 op_sel_hi:[0,0,0]
	v_mfma_scale_f32_16x16x128_f8f6f4 v[38:41], v[2:9], v[224:231], v[38:41], v234, v235 op_sel_hi:[0,0,0]
	v_mfma_scale_f32_16x16x128_f8f6f4 v[34:37], v[10:17], v[224:231], v[34:37], v234, v235 op_sel_hi:[0,0,0]
	s_setprio 0
	s_barrier
	s_add_u32 s46, s46, 0x20180
	s_addc_u32 s47, s47, 0
	s_add_u32 s37, s44, 0x200
	s_addc_u32 s74, s45, 0
	s_mov_b32 s75, 0
.LBB0_388:
	ds_read_b128 v[2:5], v180
	ds_read_b128 v[6:9], v181
	ds_read_b128 v[10:13], v182
	ds_read_b128 v[14:17], v183
	ds_read_b128 v[26:29], v184
	ds_read_b128 v[30:33], v185
	ds_read_b128 v[172:175], v186
	ds_read_b128 v[176:179], v187
	s_add_u32 s44, s46, 0xfffe0080
	s_addc_u32 s45, s47, -1
	s_cmp_eq_u32 s75, 4
	s_cselect_b32 s49, s1, s45
	s_cselect_b32 s48, s5, s44
	s_cselect_b32 s45, s23, s74
	s_cselect_b32 s44, s26, s37
	s_mov_b32 m0, s27
	v_lshl_add_u64 v[224:225], s[46:47], 0, v[168:169]
	ds_read_b128 v[18:21], v196
	ds_read_b128 v[22:25], v196 offset:1024
	ds_read_b128 v[198:201], v196 offset:2048
	ds_read_b128 v[202:205], v196 offset:3072
	ds_read_b128 v[206:209], v196 offset:4096
	ds_read_b128 v[210:213], v196 offset:5120
	ds_read_b128 v[216:219], v196 offset:6144
	ds_read_b128 v[220:223], v196 offset:7168
	global_load_lds_dwordx4 v[224:225], off
	v_lshl_add_u64 v[224:225], s[46:47], 0, v[170:171]
	s_mov_b32 m0, s35
	s_nop 0
	global_load_lds_dwordx4 v[224:225], off
	s_waitcnt vmcnt(8)
	s_waitcnt lgkmcnt(0)
	s_barrier
	s_setprio 1
	s_waitcnt lgkmcnt(0)
	v_mfma_scale_f32_16x16x128_f8f6f4 v[158:161], v[2:9], v[18:25], v[158:161], v234, v235 op_sel_hi:[0,0,0]
	v_mfma_scale_f32_16x16x128_f8f6f4 v[154:157], v[10:17], v[18:25], v[154:157], v234, v235 op_sel_hi:[0,0,0]
	v_mfma_scale_f32_16x16x128_f8f6f4 v[150:153], v[2:9], v[198:205], v[150:153], v234, v235 op_sel_hi:[0,0,0]
	v_mfma_scale_f32_16x16x128_f8f6f4 v[146:149], v[10:17], v[198:205], v[146:149], v234, v235 op_sel_hi:[0,0,0]
	v_mfma_scale_f32_16x16x128_f8f6f4 v[142:145], v[2:9], v[206:213], v[142:145], v234, v235 op_sel_hi:[0,0,0]
	v_mfma_scale_f32_16x16x128_f8f6f4 v[138:141], v[10:17], v[206:213], v[138:141], v234, v235 op_sel_hi:[0,0,0]
	v_mfma_scale_f32_16x16x128_f8f6f4 v[134:137], v[2:9], v[216:223], v[134:137], v234, v235 op_sel_hi:[0,0,0]
	v_mfma_scale_f32_16x16x128_f8f6f4 v[130:133], v[10:17], v[216:223], v[130:133], v234, v235 op_sel_hi:[0,0,0]
	s_setprio 0
	s_setprio 1
	v_mfma_scale_f32_16x16x128_f8f6f4 v[126:129], v[26:33], v[18:25], v[126:129], v234, v235 op_sel_hi:[0,0,0]
	v_mfma_scale_f32_16x16x128_f8f6f4 v[122:125], v[172:179], v[18:25], v[122:125], v234, v235 op_sel_hi:[0,0,0]
	v_mfma_scale_f32_16x16x128_f8f6f4 v[118:121], v[26:33], v[198:205], v[118:121], v234, v235 op_sel_hi:[0,0,0]
	v_mfma_scale_f32_16x16x128_f8f6f4 v[114:117], v[172:179], v[198:205], v[114:117], v234, v235 op_sel_hi:[0,0,0]
	v_mfma_scale_f32_16x16x128_f8f6f4 v[110:113], v[26:33], v[206:213], v[110:113], v234, v235 op_sel_hi:[0,0,0]
	v_mfma_scale_f32_16x16x128_f8f6f4 v[106:109], v[172:179], v[206:213], v[106:109], v234, v235 op_sel_hi:[0,0,0]
	v_mfma_scale_f32_16x16x128_f8f6f4 v[102:105], v[26:33], v[216:223], v[102:105], v234, v235 op_sel_hi:[0,0,0]
	v_mfma_scale_f32_16x16x128_f8f6f4 v[98:101], v[172:179], v[216:223], v[98:101], v234, v235 op_sel_hi:[0,0,0]
	s_setprio 0
	s_nop 7
	s_mov_b32 m0, s58
	v_lshl_add_u64 v[18:19], s[44:45], 0, v[0:1]
	s_add_u32 vcc_lo, s44, 0x20000
	global_load_lds_dwordx4 v[18:19], off
	v_lshl_add_u64 v[20:21], s[44:45], 0, v[166:167]
	s_mov_b32 m0, s59
	s_addc_u32 vcc_hi, s45, 0
	global_load_lds_dwordx4 v[20:21], off
	v_lshl_add_u64 v[22:23], vcc, 0, v[0:1]
	s_mov_b32 m0, s60
	v_lshl_add_u64 v[24:25], s[48:49], 0, v[164:165]
	global_load_lds_dwordx4 v[22:23], off
	v_lshl_add_u64 v[22:23], vcc, 0, v[166:167]
	s_mov_b32 m0, s61
	s_nop 0
	global_load_lds_dwordx4 v[22:23], off
	v_lshl_add_u64 v[22:23], s[48:49], 0, v[162:163]
	s_mov_b32 m0, s57
	s_nop 0
	global_load_lds_dwordx4 v[22:23], off
	s_mov_b32 m0, s62
	s_nop 0
	global_load_lds_dwordx4 v[24:25], off
	s_barrier
	ds_read_b128 v[198:201], v196 offset:16384
	ds_read_b128 v[202:205], v196 offset:17408
	ds_read_b128 v[206:209], v196 offset:18432
	ds_read_b128 v[210:213], v196 offset:19456
	ds_read_b128 v[216:219], v196 offset:20480
	ds_read_b128 v[220:223], v196 offset:21504
	ds_read_b128 v[224:227], v196 offset:22528
	ds_read_b128 v[228:231], v196 offset:23552
	s_waitcnt vmcnt(8)
	s_waitcnt lgkmcnt(0)
	s_barrier
	s_setprio 1
	s_waitcnt lgkmcnt(0)
	v_mfma_scale_f32_16x16x128_f8f6f4 v[94:97], v[2:9], v[198:205], v[94:97], v234, v235 op_sel_hi:[0,0,0]
	v_mfma_scale_f32_16x16x128_f8f6f4 v[90:93], v[10:17], v[198:205], v[90:93], v234, v235 op_sel_hi:[0,0,0]
	v_mfma_scale_f32_16x16x128_f8f6f4 v[86:89], v[2:9], v[206:213], v[86:89], v234, v235 op_sel_hi:[0,0,0]
	v_mfma_scale_f32_16x16x128_f8f6f4 v[82:85], v[10:17], v[206:213], v[82:85], v234, v235 op_sel_hi:[0,0,0]
	v_mfma_scale_f32_16x16x128_f8f6f4 v[78:81], v[2:9], v[216:223], v[78:81], v234, v235 op_sel_hi:[0,0,0]
	v_mfma_scale_f32_16x16x128_f8f6f4 v[74:77], v[10:17], v[216:223], v[74:77], v234, v235 op_sel_hi:[0,0,0]
	v_mfma_scale_f32_16x16x128_f8f6f4 v[70:73], v[2:9], v[224:231], v[70:73], v234, v235 op_sel_hi:[0,0,0]
	v_mfma_scale_f32_16x16x128_f8f6f4 v[66:69], v[10:17], v[224:231], v[66:69], v234, v235 op_sel_hi:[0,0,0]
	s_setprio 0
	s_setprio 1
	v_mfma_scale_f32_16x16x128_f8f6f4 v[62:65], v[26:33], v[198:205], v[62:65], v234, v235 op_sel_hi:[0,0,0]
	v_mfma_scale_f32_16x16x128_f8f6f4 v[58:61], v[172:179], v[198:205], v[58:61], v234, v235 op_sel_hi:[0,0,0]
	v_mfma_scale_f32_16x16x128_f8f6f4 v[54:57], v[26:33], v[206:213], v[54:57], v234, v235 op_sel_hi:[0,0,0]
	v_mfma_scale_f32_16x16x128_f8f6f4 v[50:53], v[172:179], v[206:213], v[50:53], v234, v235 op_sel_hi:[0,0,0]
	v_mfma_scale_f32_16x16x128_f8f6f4 v[46:49], v[26:33], v[216:223], v[46:49], v234, v235 op_sel_hi:[0,0,0]
	v_mfma_scale_f32_16x16x128_f8f6f4 v[42:45], v[172:179], v[216:223], v[42:45], v234, v235 op_sel_hi:[0,0,0]
	v_mfma_scale_f32_16x16x128_f8f6f4 v[38:41], v[26:33], v[224:231], v[38:41], v234, v235 op_sel_hi:[0,0,0]
	v_mfma_scale_f32_16x16x128_f8f6f4 v[34:37], v[172:179], v[224:231], v[34:37], v234, v235 op_sel_hi:[0,0,0]
	s_setprio 0
	s_nop 7
	s_add_u32 s48, s48, 0x20000
	s_addc_u32 s49, s49, 0
	s_mov_b32 m0, s63
	v_lshl_add_u64 v[232:233], s[48:49], 0, v[162:163]
	global_load_lds_dwordx4 v[232:233], off
	v_lshl_add_u64 v[232:233], s[48:49], 0, v[164:165]
	s_mov_b32 m0, s64
	s_nop 0
	global_load_lds_dwordx4 v[232:233], off
	s_barrier
	ds_read_b128 v[10:13], v188
	ds_read_b128 v[14:17], v189
	ds_read_b128 v[26:29], v190
	ds_read_b128 v[30:33], v191
	ds_read_b128 v[2:5], v192
	ds_read_b128 v[6:9], v193
	ds_read_b128 v[172:175], v194
	ds_read_b128 v[176:179], v195
	ds_read_b128 v[198:201], v196 offset:32768
	ds_read_b128 v[202:205], v196 offset:33792
	ds_read_b128 v[206:209], v196 offset:34816
	ds_read_b128 v[210:213], v196 offset:35840
	ds_read_b128 v[216:219], v196 offset:36864
	ds_read_b128 v[220:223], v196 offset:37888
	ds_read_b128 v[224:227], v196 offset:38912
	ds_read_b128 v[228:231], v196 offset:39936
	s_waitcnt vmcnt(8)
	s_waitcnt lgkmcnt(0)
	s_barrier
	s_setprio 1
	s_waitcnt lgkmcnt(0)
	v_mfma_scale_f32_16x16x128_f8f6f4 v[158:161], v[10:17], v[198:205], v[158:161], v234, v235 op_sel_hi:[0,0,0]
	v_mfma_scale_f32_16x16x128_f8f6f4 v[154:157], v[26:33], v[198:205], v[154:157], v234, v235 op_sel_hi:[0,0,0]
	v_mfma_scale_f32_16x16x128_f8f6f4 v[150:153], v[10:17], v[206:213], v[150:153], v234, v235 op_sel_hi:[0,0,0]
	v_mfma_scale_f32_16x16x128_f8f6f4 v[146:149], v[26:33], v[206:213], v[146:149], v234, v235 op_sel_hi:[0,0,0]
	v_mfma_scale_f32_16x16x128_f8f6f4 v[142:145], v[10:17], v[216:223], v[142:145], v234, v235 op_sel_hi:[0,0,0]
	v_mfma_scale_f32_16x16x128_f8f6f4 v[138:141], v[26:33], v[216:223], v[138:141], v234, v235 op_sel_hi:[0,0,0]
	v_mfma_scale_f32_16x16x128_f8f6f4 v[134:137], v[10:17], v[224:231], v[134:137], v234, v235 op_sel_hi:[0,0,0]
	v_mfma_scale_f32_16x16x128_f8f6f4 v[130:133], v[26:33], v[224:231], v[130:133], v234, v235 op_sel_hi:[0,0,0]
	s_setprio 0
	s_setprio 1
	v_mfma_scale_f32_16x16x128_f8f6f4 v[126:129], v[2:9], v[198:205], v[126:129], v234, v235 op_sel_hi:[0,0,0]
	v_mfma_scale_f32_16x16x128_f8f6f4 v[122:125], v[172:179], v[198:205], v[122:125], v234, v235 op_sel_hi:[0,0,0]
	v_mfma_scale_f32_16x16x128_f8f6f4 v[118:121], v[2:9], v[206:213], v[118:121], v234, v235 op_sel_hi:[0,0,0]
	v_mfma_scale_f32_16x16x128_f8f6f4 v[114:117], v[172:179], v[206:213], v[114:117], v234, v235 op_sel_hi:[0,0,0]
	v_mfma_scale_f32_16x16x128_f8f6f4 v[110:113], v[2:9], v[216:223], v[110:113], v234, v235 op_sel_hi:[0,0,0]
	v_mfma_scale_f32_16x16x128_f8f6f4 v[106:109], v[172:179], v[216:223], v[106:109], v234, v235 op_sel_hi:[0,0,0]
	v_mfma_scale_f32_16x16x128_f8f6f4 v[102:105], v[2:9], v[224:231], v[102:105], v234, v235 op_sel_hi:[0,0,0]
	v_mfma_scale_f32_16x16x128_f8f6f4 v[98:101], v[172:179], v[224:231], v[98:101], v234, v235 op_sel_hi:[0,0,0]
	s_setprio 0
	s_nop 7
	s_mov_b32 m0, s7
	v_lshl_add_u64 v[18:19], v[18:19], 0, s[66:67]
	s_add_u32 s44, s44, 0x20080
	global_load_lds_dwordx4 v[18:19], off
	v_lshl_add_u64 v[18:19], v[20:21], 0, s[66:67]
	s_mov_b32 m0, s65
	s_addc_u32 s45, s45, 0
	global_load_lds_dwordx4 v[18:19], off
	v_lshl_add_u64 v[18:19], s[44:45], 0, v[0:1]
	s_mov_b32 m0, s13
	s_nop 0
	global_load_lds_dwordx4 v[18:19], off
	v_lshl_add_u64 v[18:19], s[44:45], 0, v[166:167]
	s_mov_b32 m0, s51
	s_nop 0
	global_load_lds_dwordx4 v[18:19], off
	v_lshl_add_u64 v[18:19], v[22:23], 0, s[66:67]
	s_mov_b32 m0, s68
	s_nop 0
	global_load_lds_dwordx4 v[18:19], off
	v_lshl_add_u64 v[18:19], v[24:25], 0, s[66:67]
	s_mov_b32 m0, s52
	s_nop 0
	global_load_lds_dwordx4 v[18:19], off
	s_barrier
	ds_read_b128 v[198:201], v196 offset:49152
	ds_read_b128 v[202:205], v196 offset:50176
	ds_read_b128 v[206:209], v196 offset:51200
	ds_read_b128 v[210:213], v196 offset:52224
	ds_read_b128 v[216:219], v196 offset:53248
	ds_read_b128 v[220:223], v196 offset:54272
	ds_read_b128 v[224:227], v196 offset:55296
	ds_read_b128 v[228:231], v196 offset:56320
	s_waitcnt vmcnt(8)
	s_waitcnt lgkmcnt(0)
	s_barrier
	s_setprio 1
	s_waitcnt lgkmcnt(0)
	v_mfma_scale_f32_16x16x128_f8f6f4 v[94:97], v[10:17], v[198:205], v[94:97], v234, v235 op_sel_hi:[0,0,0]
	v_mfma_scale_f32_16x16x128_f8f6f4 v[90:93], v[26:33], v[198:205], v[90:93], v234, v235 op_sel_hi:[0,0,0]
	v_mfma_scale_f32_16x16x128_f8f6f4 v[86:89], v[10:17], v[206:213], v[86:89], v234, v235 op_sel_hi:[0,0,0]
	v_mfma_scale_f32_16x16x128_f8f6f4 v[82:85], v[26:33], v[206:213], v[82:85], v234, v235 op_sel_hi:[0,0,0]
	v_mfma_scale_f32_16x16x128_f8f6f4 v[78:81], v[10:17], v[216:223], v[78:81], v234, v235 op_sel_hi:[0,0,0]
	v_mfma_scale_f32_16x16x128_f8f6f4 v[74:77], v[26:33], v[216:223], v[74:77], v234, v235 op_sel_hi:[0,0,0]
	v_mfma_scale_f32_16x16x128_f8f6f4 v[70:73], v[10:17], v[224:231], v[70:73], v234, v235 op_sel_hi:[0,0,0]
	v_mfma_scale_f32_16x16x128_f8f6f4 v[66:69], v[26:33], v[224:231], v[66:69], v234, v235 op_sel_hi:[0,0,0]
	s_setprio 0
	s_setprio 1
	v_mfma_scale_f32_16x16x128_f8f6f4 v[62:65], v[2:9], v[198:205], v[62:65], v234, v235 op_sel_hi:[0,0,0]
	v_mfma_scale_f32_16x16x128_f8f6f4 v[58:61], v[172:179], v[198:205], v[58:61], v234, v235 op_sel_hi:[0,0,0]
	v_mfma_scale_f32_16x16x128_f8f6f4 v[54:57], v[2:9], v[206:213], v[54:57], v234, v235 op_sel_hi:[0,0,0]
	v_mfma_scale_f32_16x16x128_f8f6f4 v[50:53], v[172:179], v[206:213], v[50:53], v234, v235 op_sel_hi:[0,0,0]
	v_mfma_scale_f32_16x16x128_f8f6f4 v[46:49], v[2:9], v[216:223], v[46:49], v234, v235 op_sel_hi:[0,0,0]
	v_mfma_scale_f32_16x16x128_f8f6f4 v[42:45], v[172:179], v[216:223], v[42:45], v234, v235 op_sel_hi:[0,0,0]
	v_mfma_scale_f32_16x16x128_f8f6f4 v[38:41], v[2:9], v[224:231], v[38:41], v234, v235 op_sel_hi:[0,0,0]
	v_mfma_scale_f32_16x16x128_f8f6f4 v[34:37], v[172:179], v[224:231], v[34:37], v234, v235 op_sel_hi:[0,0,0]
	s_setprio 0
	s_barrier
	s_add_i32 s75, s75, 2
	s_add_u32 s46, s46, 0x100
	s_addc_u32 s47, s47, 0
	s_add_u32 s37, s37, 0x100
	s_addc_u32 s74, s74, 0
	s_cmp_gt_u32 s75, 5
	s_cbranch_scc0 .LBB0_388
	s_branch .Lip8_join

.Lrw_done_g1_0:
	s_waitcnt lgkmcnt(0)
	v_mov_b32_e32 v169, v1
	s_barrier
	s_setprio 1
	s_waitcnt lgkmcnt(0)
	v_mfma_scale_f32_16x16x128_f8f6f4 v[150:153], v[26:33], v[198:205], 0, v234, v235 op_sel_hi:[0,0,0]
	v_mfma_scale_f32_16x16x128_f8f6f4 v[146:149], v[18:25], v[198:205], 0, v234, v235 op_sel_hi:[0,0,0]
	v_mfma_scale_f32_16x16x128_f8f6f4 v[142:145], v[26:33], v[206:213], 0, v234, v235 op_sel_hi:[0,0,0]
	v_mfma_scale_f32_16x16x128_f8f6f4 v[138:141], v[18:25], v[206:213], 0, v234, v235 op_sel_hi:[0,0,0]
	v_mfma_scale_f32_16x16x128_f8f6f4 v[134:137], v[26:33], v[216:223], 0, v234, v235 op_sel_hi:[0,0,0]
	v_mfma_scale_f32_16x16x128_f8f6f4 v[130:133], v[18:25], v[216:223], 0, v234, v235 op_sel_hi:[0,0,0]
	v_mfma_scale_f32_16x16x128_f8f6f4 v[126:129], v[26:33], v[224:231], 0, v234, v235 op_sel_hi:[0,0,0]
	v_mfma_scale_f32_16x16x128_f8f6f4 v[122:125], v[18:25], v[224:231], 0, v234, v235 op_sel_hi:[0,0,0]
	s_setprio 0
	s_setprio 1
	v_mfma_scale_f32_16x16x128_f8f6f4 v[118:121], v[10:17], v[198:205], 0, v234, v235 op_sel_hi:[0,0,0]
	v_mfma_scale_f32_16x16x128_f8f6f4 v[114:117], v[2:9], v[198:205], 0, v234, v235 op_sel_hi:[0,0,0]
	v_mfma_scale_f32_16x16x128_f8f6f4 v[110:113], v[10:17], v[206:213], 0, v234, v235 op_sel_hi:[0,0,0]
	v_mfma_scale_f32_16x16x128_f8f6f4 v[106:109], v[2:9], v[206:213], 0, v234, v235 op_sel_hi:[0,0,0]
	v_mfma_scale_f32_16x16x128_f8f6f4 v[102:105], v[10:17], v[216:223], 0, v234, v235 op_sel_hi:[0,0,0]
	v_mfma_scale_f32_16x16x128_f8f6f4 v[98:101], v[2:9], v[216:223], 0, v234, v235 op_sel_hi:[0,0,0]
	v_mfma_scale_f32_16x16x128_f8f6f4 v[94:97], v[10:17], v[224:231], 0, v234, v235 op_sel_hi:[0,0,0]
	v_mfma_scale_f32_16x16x128_f8f6f4 v[90:93], v[2:9], v[224:231], 0, v234, v235 op_sel_hi:[0,0,0]
	s_setprio 0
	s_nop 7
	v_lshl_add_u64 v[170:171], s[4:5], 0, v[162:163]
	s_mov_b64 s[54:55], 0x100
	s_mov_b32 m0, s68
	v_lshl_add_u64 v[172:173], v[170:171], 0, s[54:55]
	global_load_lds_dwordx4 v[172:173], off
	v_lshl_add_u64 v[172:173], s[4:5], 0, v[164:165]
	v_lshl_add_u64 v[232:233], v[172:173], 0, s[54:55]
	s_add_u32 s54, s4, 0x20100
	s_mov_b32 m0, s60
	s_addc_u32 s55, s5, 0
	global_load_lds_dwordx4 v[232:233], off
	v_lshl_add_u64 v[232:233], s[54:55], 0, v[162:163]
	s_mov_b32 m0, s61
	v_lshlrev_b32_e32 v0, 10, v195
	global_load_lds_dwordx4 v[232:233], off
	v_lshl_add_u64 v[232:233], s[54:55], 0, v[164:165]
	s_mov_b32 m0, s62
	v_and_or_b32 v0, v0, s82, v174
	global_load_lds_dwordx4 v[232:233], off
	v_bfe_u32 v197, v195, 16, 16
	s_mov_b32 m0, s65
	v_lshl_add_u32 v197, v197, 10, v175
	global_load_lds_dwordx4 v0, s[34:35]
	s_mov_b32 m0, s63
	s_nop 0
	global_load_lds_dwordx4 v197, s[34:35]
	s_barrier
	ds_read_b128 v[198:201], v192 offset:16384
	ds_read_b128 v[202:205], v192 offset:17408
	ds_read_b128 v[206:209], v192 offset:18432
	ds_read_b128 v[210:213], v192 offset:19456
	ds_read_b128 v[216:219], v192 offset:20480
	ds_read_b128 v[220:223], v192 offset:21504
	ds_read_b128 v[224:227], v192 offset:22528
	ds_read_b128 v[228:231], v192 offset:23552
	s_cmp_eq_u32 s23, 0
	s_cbranch_scc1 .Lrw_first_g1_1
	s_waitcnt vmcnt(12)
	s_branch .Lrw_done_g1_1

.Lrw_done_g1_1:
	s_waitcnt lgkmcnt(0)
	s_barrier
	s_setprio 1
	s_waitcnt lgkmcnt(0)
	v_mfma_scale_f32_16x16x128_f8f6f4 v[86:89], v[26:33], v[198:205], 0, v234, v235 op_sel_hi:[0,0,0]
	v_mfma_scale_f32_16x16x128_f8f6f4 v[82:85], v[18:25], v[198:205], 0, v234, v235 op_sel_hi:[0,0,0]
	v_mfma_scale_f32_16x16x128_f8f6f4 v[78:81], v[26:33], v[206:213], 0, v234, v235 op_sel_hi:[0,0,0]
	v_mfma_scale_f32_16x16x128_f8f6f4 v[74:77], v[18:25], v[206:213], 0, v234, v235 op_sel_hi:[0,0,0]
	v_mfma_scale_f32_16x16x128_f8f6f4 v[70:73], v[26:33], v[216:223], 0, v234, v235 op_sel_hi:[0,0,0]
	v_mfma_scale_f32_16x16x128_f8f6f4 v[66:69], v[18:25], v[216:223], 0, v234, v235 op_sel_hi:[0,0,0]
	v_mfma_scale_f32_16x16x128_f8f6f4 v[62:65], v[26:33], v[224:231], 0, v234, v235 op_sel_hi:[0,0,0]
	v_mfma_scale_f32_16x16x128_f8f6f4 v[58:61], v[18:25], v[224:231], 0, v234, v235 op_sel_hi:[0,0,0]
	s_setprio 0
	s_setprio 1
	v_mfma_scale_f32_16x16x128_f8f6f4 v[54:57], v[10:17], v[198:205], 0, v234, v235 op_sel_hi:[0,0,0]
	v_mfma_scale_f32_16x16x128_f8f6f4 v[50:53], v[2:9], v[198:205], 0, v234, v235 op_sel_hi:[0,0,0]
	v_mfma_scale_f32_16x16x128_f8f6f4 v[46:49], v[10:17], v[206:213], 0, v234, v235 op_sel_hi:[0,0,0]
	v_mfma_scale_f32_16x16x128_f8f6f4 v[42:45], v[2:9], v[206:213], 0, v234, v235 op_sel_hi:[0,0,0]
	v_mfma_scale_f32_16x16x128_f8f6f4 v[38:41], v[10:17], v[216:223], 0, v234, v235 op_sel_hi:[0,0,0]
	v_mfma_scale_f32_16x16x128_f8f6f4 v[34:37], v[2:9], v[216:223], 0, v234, v235 op_sel_hi:[0,0,0]
	v_mfma_scale_f32_16x16x128_f8f6f4 v[154:157], v[10:17], v[224:231], 0, v234, v235 op_sel_hi:[0,0,0]
	v_mfma_scale_f32_16x16x128_f8f6f4 v[158:161], v[2:9], v[224:231], 0, v234, v235 op_sel_hi:[0,0,0]
	s_setprio 0
	s_nop 7
	s_mov_b32 m0, s10
	s_nop 0
	global_load_lds_dwordx4 v166, s[34:35]
	s_mov_b32 m0, s11
	s_nop 0
	global_load_lds_dwordx4 v168, s[34:35]
	s_barrier
	ds_read_b128 v[18:21], v184
	ds_read_b128 v[22:25], v185
	ds_read_b128 v[26:29], v186
	ds_read_b128 v[30:33], v187
	ds_read_b128 v[2:5], v188
	ds_read_b128 v[6:9], v189
	ds_read_b128 v[10:13], v190
	ds_read_b128 v[14:17], v191
	ds_read_b128 v[198:201], v192 offset:32768
	ds_read_b128 v[202:205], v192 offset:33792
	ds_read_b128 v[206:209], v192 offset:34816
	ds_read_b128 v[210:213], v192 offset:35840
	ds_read_b128 v[216:219], v192 offset:36864
	ds_read_b128 v[220:223], v192 offset:37888
	ds_read_b128 v[224:227], v192 offset:38912
	ds_read_b128 v[228:231], v192 offset:39936
	s_waitcnt vmcnt(8)
	s_waitcnt lgkmcnt(0)
	s_barrier
	s_setprio 1
	s_waitcnt lgkmcnt(0)
	v_mfma_scale_f32_16x16x128_f8f6f4 v[150:153], v[18:25], v[198:205], v[150:153], v234, v235 op_sel_hi:[0,0,0]
	v_mfma_scale_f32_16x16x128_f8f6f4 v[146:149], v[26:33], v[198:205], v[146:149], v234, v235 op_sel_hi:[0,0,0]
	v_mfma_scale_f32_16x16x128_f8f6f4 v[142:145], v[18:25], v[206:213], v[142:145], v234, v235 op_sel_hi:[0,0,0]
	v_mfma_scale_f32_16x16x128_f8f6f4 v[138:141], v[26:33], v[206:213], v[138:141], v234, v235 op_sel_hi:[0,0,0]
	v_mfma_scale_f32_16x16x128_f8f6f4 v[134:137], v[18:25], v[216:223], v[134:137], v234, v235 op_sel_hi:[0,0,0]
	v_mfma_scale_f32_16x16x128_f8f6f4 v[130:133], v[26:33], v[216:223], v[130:133], v234, v235 op_sel_hi:[0,0,0]
	v_mfma_scale_f32_16x16x128_f8f6f4 v[126:129], v[18:25], v[224:231], v[126:129], v234, v235 op_sel_hi:[0,0,0]
	v_mfma_scale_f32_16x16x128_f8f6f4 v[122:125], v[26:33], v[224:231], v[122:125], v234, v235 op_sel_hi:[0,0,0]
	s_setprio 0
	s_setprio 1
	v_mfma_scale_f32_16x16x128_f8f6f4 v[118:121], v[2:9], v[198:205], v[118:121], v234, v235 op_sel_hi:[0,0,0]
	v_mfma_scale_f32_16x16x128_f8f6f4 v[114:117], v[10:17], v[198:205], v[114:117], v234, v235 op_sel_hi:[0,0,0]
	v_mfma_scale_f32_16x16x128_f8f6f4 v[110:113], v[2:9], v[206:213], v[110:113], v234, v235 op_sel_hi:[0,0,0]
	v_mfma_scale_f32_16x16x128_f8f6f4 v[106:109], v[10:17], v[206:213], v[106:109], v234, v235 op_sel_hi:[0,0,0]
	v_mfma_scale_f32_16x16x128_f8f6f4 v[102:105], v[2:9], v[216:223], v[102:105], v234, v235 op_sel_hi:[0,0,0]
	v_mfma_scale_f32_16x16x128_f8f6f4 v[98:101], v[10:17], v[216:223], v[98:101], v234, v235 op_sel_hi:[0,0,0]
	v_mfma_scale_f32_16x16x128_f8f6f4 v[94:97], v[2:9], v[224:231], v[94:97], v234, v235 op_sel_hi:[0,0,0]
	v_mfma_scale_f32_16x16x128_f8f6f4 v[90:93], v[10:17], v[224:231], v[90:93], v234, v235 op_sel_hi:[0,0,0]
	s_setprio 0
	s_nop 7
	s_mov_b64 s[54:55], 0x180
	s_mov_b32 m0, s64
	v_lshl_add_u64 v[170:171], v[170:171], 0, s[54:55]
	global_load_lds_dwordx4 v[170:171], off
	v_lshl_add_u64 v[170:171], v[172:173], 0, s[54:55]
	s_add_u32 s54, s4, 0x20180
	s_mov_b32 m0, s81
	s_addc_u32 s55, s5, 0
	global_load_lds_dwordx4 v[170:171], off
	v_lshl_add_u64 v[170:171], s[54:55], 0, v[162:163]
	s_mov_b32 m0, s49
	s_nop 0
	global_load_lds_dwordx4 v[170:171], off
	v_lshl_add_u64 v[170:171], s[54:55], 0, v[164:165]
	s_mov_b32 m0, s30
	s_nop 0
	global_load_lds_dwordx4 v[170:171], off
	s_mov_b32 m0, s6
	s_nop 0
	global_load_lds_dwordx4 v0, s[36:37]
	s_mov_b32 m0, s7
	s_nop 0
	global_load_lds_dwordx4 v197, s[36:37]
	s_barrier
	ds_read_b128 v[198:201], v192 offset:49152
	ds_read_b128 v[202:205], v192 offset:50176
	ds_read_b128 v[206:209], v192 offset:51200
	ds_read_b128 v[210:213], v192 offset:52224
	ds_read_b128 v[216:219], v192 offset:53248
	ds_read_b128 v[220:223], v192 offset:54272
	ds_read_b128 v[224:227], v192 offset:55296
	ds_read_b128 v[228:231], v192 offset:56320
	s_waitcnt vmcnt(8)
	s_waitcnt lgkmcnt(0)
	s_barrier
	s_setprio 1
	s_waitcnt lgkmcnt(0)
	v_mfma_scale_f32_16x16x128_f8f6f4 v[86:89], v[18:25], v[198:205], v[86:89], v234, v235 op_sel_hi:[0,0,0]
	v_mfma_scale_f32_16x16x128_f8f6f4 v[82:85], v[26:33], v[198:205], v[82:85], v234, v235 op_sel_hi:[0,0,0]
	v_mfma_scale_f32_16x16x128_f8f6f4 v[78:81], v[18:25], v[206:213], v[78:81], v234, v235 op_sel_hi:[0,0,0]
	v_mfma_scale_f32_16x16x128_f8f6f4 v[74:77], v[26:33], v[206:213], v[74:77], v234, v235 op_sel_hi:[0,0,0]
	v_mfma_scale_f32_16x16x128_f8f6f4 v[70:73], v[18:25], v[216:223], v[70:73], v234, v235 op_sel_hi:[0,0,0]
	v_mfma_scale_f32_16x16x128_f8f6f4 v[66:69], v[26:33], v[216:223], v[66:69], v234, v235 op_sel_hi:[0,0,0]
	v_mfma_scale_f32_16x16x128_f8f6f4 v[62:65], v[18:25], v[224:231], v[62:65], v234, v235 op_sel_hi:[0,0,0]
	v_mfma_scale_f32_16x16x128_f8f6f4 v[58:61], v[26:33], v[224:231], v[58:61], v234, v235 op_sel_hi:[0,0,0]
	s_setprio 0
	s_setprio 1
	v_mfma_scale_f32_16x16x128_f8f6f4 v[54:57], v[2:9], v[198:205], v[54:57], v234, v235 op_sel_hi:[0,0,0]
	v_mfma_scale_f32_16x16x128_f8f6f4 v[50:53], v[10:17], v[198:205], v[50:53], v234, v235 op_sel_hi:[0,0,0]
	v_mfma_scale_f32_16x16x128_f8f6f4 v[46:49], v[2:9], v[206:213], v[46:49], v234, v235 op_sel_hi:[0,0,0]
	v_mfma_scale_f32_16x16x128_f8f6f4 v[42:45], v[10:17], v[206:213], v[42:45], v234, v235 op_sel_hi:[0,0,0]
	v_mfma_scale_f32_16x16x128_f8f6f4 v[38:41], v[2:9], v[216:223], v[38:41], v234, v235 op_sel_hi:[0,0,0]
	v_mfma_scale_f32_16x16x128_f8f6f4 v[34:37], v[10:17], v[216:223], v[34:37], v234, v235 op_sel_hi:[0,0,0]
	v_mfma_scale_f32_16x16x128_f8f6f4 v[154:157], v[2:9], v[224:231], v[154:157], v234, v235 op_sel_hi:[0,0,0]
	v_mfma_scale_f32_16x16x128_f8f6f4 v[158:161], v[10:17], v[224:231], v[158:161], v234, v235 op_sel_hi:[0,0,0]
	s_setprio 0
	s_barrier
	s_add_u32 s43, s4, 0x200
	s_addc_u32 s45, s5, 0
	s_mov_b32 s74, 0
	s_mov_b64 s[54:55], s[36:37]
	s_branch .LBB0_2003
.LBB0_2002:
	ds_read_b128 v[2:5], v183
	ds_read_b128 v[6:9], v182
	ds_read_b128 v[10:13], v181
	ds_read_b128 v[14:17], v180
	ds_read_b128 v[26:29], v179
	ds_read_b128 v[30:33], v178
	ds_read_b128 v[198:201], v177
	ds_read_b128 v[202:205], v176
	s_add_u32 s58, s54, 0x80
	s_addc_u32 s59, s55, 0
	s_and_b64 s[56:57], s[4:5], exec
	s_cselect_b32 s59, s9, s59
	s_cselect_b32 s58, s8, s58
	s_cselect_b32 s57, s47, s45
	s_cselect_b32 s56, s46, s43
	s_mov_b32 m0, s27
	v_lshl_add_u64 v[170:171], s[54:55], 0, v[166:167]
	ds_read_b128 v[18:21], v192
	ds_read_b128 v[22:25], v192 offset:1024
	ds_read_b128 v[206:209], v192 offset:2048
	ds_read_b128 v[210:213], v192 offset:3072
	ds_read_b128 v[216:219], v192 offset:4096
	ds_read_b128 v[220:223], v192 offset:5120
	ds_read_b128 v[224:227], v192 offset:6144
	ds_read_b128 v[228:231], v192 offset:7168
	global_load_lds_dwordx4 v[170:171], off
	v_lshl_add_u64 v[170:171], s[54:55], 0, v[168:169]
	s_mov_b32 m0, s41
	s_nop 0
	global_load_lds_dwordx4 v[170:171], off
	s_waitcnt vmcnt(8)
	s_waitcnt lgkmcnt(0)
	s_barrier
	s_setprio 1
	s_waitcnt lgkmcnt(0)
	v_mfma_scale_f32_16x16x128_f8f6f4 v[150:153], v[2:9], v[18:25], v[150:153], v234, v235 op_sel_hi:[0,0,0]
	v_mfma_scale_f32_16x16x128_f8f6f4 v[146:149], v[10:17], v[18:25], v[146:149], v234, v235 op_sel_hi:[0,0,0]
	v_mfma_scale_f32_16x16x128_f8f6f4 v[142:145], v[2:9], v[206:213], v[142:145], v234, v235 op_sel_hi:[0,0,0]
	v_mfma_scale_f32_16x16x128_f8f6f4 v[138:141], v[10:17], v[206:213], v[138:141], v234, v235 op_sel_hi:[0,0,0]
	v_mfma_scale_f32_16x16x128_f8f6f4 v[134:137], v[2:9], v[216:223], v[134:137], v234, v235 op_sel_hi:[0,0,0]
	v_mfma_scale_f32_16x16x128_f8f6f4 v[130:133], v[10:17], v[216:223], v[130:133], v234, v235 op_sel_hi:[0,0,0]
	v_mfma_scale_f32_16x16x128_f8f6f4 v[126:129], v[2:9], v[224:231], v[126:129], v234, v235 op_sel_hi:[0,0,0]
	v_mfma_scale_f32_16x16x128_f8f6f4 v[122:125], v[10:17], v[224:231], v[122:125], v234, v235 op_sel_hi:[0,0,0]
	s_setprio 0
	s_setprio 1
	v_mfma_scale_f32_16x16x128_f8f6f4 v[118:121], v[26:33], v[18:25], v[118:121], v234, v235 op_sel_hi:[0,0,0]
	v_mfma_scale_f32_16x16x128_f8f6f4 v[114:117], v[198:205], v[18:25], v[114:117], v234, v235 op_sel_hi:[0,0,0]
	v_mfma_scale_f32_16x16x128_f8f6f4 v[110:113], v[26:33], v[206:213], v[110:113], v234, v235 op_sel_hi:[0,0,0]
	v_mfma_scale_f32_16x16x128_f8f6f4 v[106:109], v[198:205], v[206:213], v[106:109], v234, v235 op_sel_hi:[0,0,0]
	v_mfma_scale_f32_16x16x128_f8f6f4 v[102:105], v[26:33], v[216:223], v[102:105], v234, v235 op_sel_hi:[0,0,0]
	v_mfma_scale_f32_16x16x128_f8f6f4 v[98:101], v[198:205], v[216:223], v[98:101], v234, v235 op_sel_hi:[0,0,0]
	v_mfma_scale_f32_16x16x128_f8f6f4 v[94:97], v[26:33], v[224:231], v[94:97], v234, v235 op_sel_hi:[0,0,0]
	v_mfma_scale_f32_16x16x128_f8f6f4 v[90:93], v[198:205], v[224:231], v[90:93], v234, v235 op_sel_hi:[0,0,0]
	s_setprio 0
	s_nop 7
	s_mov_b32 m0, s68
	v_lshl_add_u64 v[18:19], s[56:57], 0, v[162:163]
	s_add_u32 vcc_lo, s56, 0x20000
	global_load_lds_dwordx4 v[18:19], off
	v_lshl_add_u64 v[20:21], s[56:57], 0, v[164:165]
	s_mov_b32 m0, s60
	s_addc_u32 vcc_hi, s57, 0
	global_load_lds_dwordx4 v[20:21], off
	v_lshl_add_u64 v[22:23], vcc, 0, v[162:163]
	s_mov_b32 m0, s61
	s_nop 0
	global_load_lds_dwordx4 v[22:23], off
	v_lshl_add_u64 v[22:23], vcc, 0, v[164:165]
	s_mov_b32 m0, s62
	s_nop 0
	global_load_lds_dwordx4 v[22:23], off
	v_cndmask_b32_e64 v22, v195, v193, s[4:5]
	v_lshlrev_b32_e32 v0, 10, v22
	v_and_or_b32 v0, v0, s82, v174
	v_bfe_u32 v22, v22, 16, 16
	s_mov_b32 m0, s65
	v_lshl_add_u32 v22, v22, 10, v175
	global_load_lds_dwordx4 v0, s[58:59]
	s_mov_b32 m0, s63
	v_mov_b32_e32 v23, v1
	global_load_lds_dwordx4 v22, s[58:59]
	s_barrier
	ds_read_b128 v[206:209], v192 offset:16384
	ds_read_b128 v[210:213], v192 offset:17408
	ds_read_b128 v[216:219], v192 offset:18432
	ds_read_b128 v[220:223], v192 offset:19456
	ds_read_b128 v[224:227], v192 offset:20480
	ds_read_b128 v[228:231], v192 offset:21504
	ds_read_b128 v[244:247], v192 offset:22528
	ds_read_b128 v[248:251], v192 offset:23552
	s_waitcnt vmcnt(8)
	s_waitcnt lgkmcnt(0)
	v_lshl_add_u64 v[24:25], s[58:59], 0, v[0:1]
	v_lshl_add_u64 v[22:23], s[58:59], 0, v[22:23]
	s_barrier
	s_setprio 1
	s_waitcnt lgkmcnt(0)
	v_mfma_scale_f32_16x16x128_f8f6f4 v[86:89], v[2:9], v[206:213], v[86:89], v234, v235 op_sel_hi:[0,0,0]
	v_mfma_scale_f32_16x16x128_f8f6f4 v[82:85], v[10:17], v[206:213], v[82:85], v234, v235 op_sel_hi:[0,0,0]
	v_mfma_scale_f32_16x16x128_f8f6f4 v[78:81], v[2:9], v[216:223], v[78:81], v234, v235 op_sel_hi:[0,0,0]
	v_mfma_scale_f32_16x16x128_f8f6f4 v[74:77], v[10:17], v[216:223], v[74:77], v234, v235 op_sel_hi:[0,0,0]
	v_mfma_scale_f32_16x16x128_f8f6f4 v[70:73], v[2:9], v[224:231], v[70:73], v234, v235 op_sel_hi:[0,0,0]
	v_mfma_scale_f32_16x16x128_f8f6f4 v[66:69], v[10:17], v[224:231], v[66:69], v234, v235 op_sel_hi:[0,0,0]
	v_mfma_scale_f32_16x16x128_f8f6f4 v[62:65], v[2:9], v[244:251], v[62:65], v234, v235 op_sel_hi:[0,0,0]
	v_mfma_scale_f32_16x16x128_f8f6f4 v[58:61], v[10:17], v[244:251], v[58:61], v234, v235 op_sel_hi:[0,0,0]
	s_setprio 0
	s_setprio 1
	v_mfma_scale_f32_16x16x128_f8f6f4 v[54:57], v[26:33], v[206:213], v[54:57], v234, v235 op_sel_hi:[0,0,0]
	v_mfma_scale_f32_16x16x128_f8f6f4 v[50:53], v[198:205], v[206:213], v[50:53], v234, v235 op_sel_hi:[0,0,0]
	v_mfma_scale_f32_16x16x128_f8f6f4 v[46:49], v[26:33], v[216:223], v[46:49], v234, v235 op_sel_hi:[0,0,0]
	v_mfma_scale_f32_16x16x128_f8f6f4 v[42:45], v[198:205], v[216:223], v[42:45], v234, v235 op_sel_hi:[0,0,0]
	v_mfma_scale_f32_16x16x128_f8f6f4 v[38:41], v[26:33], v[224:231], v[38:41], v234, v235 op_sel_hi:[0,0,0]
	v_mfma_scale_f32_16x16x128_f8f6f4 v[34:37], v[198:205], v[224:231], v[34:37], v234, v235 op_sel_hi:[0,0,0]
	v_mfma_scale_f32_16x16x128_f8f6f4 v[154:157], v[26:33], v[244:251], v[154:157], v234, v235 op_sel_hi:[0,0,0]
	v_mfma_scale_f32_16x16x128_f8f6f4 v[158:161], v[198:205], v[244:251], v[158:161], v234, v235 op_sel_hi:[0,0,0]
	s_setprio 0
	s_nop 7
	v_cndmask_b32_e64 v0, v196, v194, s[4:5]
	v_lshlrev_b32_e32 v170, 10, v0
	s_mov_b32 m0, s10
	v_and_or_b32 v170, v170, s82, v174
	v_bfe_u32 v0, v0, 16, 16
	v_lshl_add_u32 v0, v0, 10, v175
	global_load_lds_dwordx4 v170, s[58:59]
	s_mov_b32 m0, s11
	s_nop 0
	global_load_lds_dwordx4 v0, s[58:59]
	s_barrier
	ds_read_b128 v[10:13], v184
	ds_read_b128 v[14:17], v185
	ds_read_b128 v[26:29], v186
	ds_read_b128 v[30:33], v187
	ds_read_b128 v[2:5], v188
	ds_read_b128 v[6:9], v189
	ds_read_b128 v[198:201], v190
	ds_read_b128 v[202:205], v191
	ds_read_b128 v[206:209], v192 offset:32768
	ds_read_b128 v[210:213], v192 offset:33792
	ds_read_b128 v[216:219], v192 offset:34816
	ds_read_b128 v[220:223], v192 offset:35840
	ds_read_b128 v[224:227], v192 offset:36864
	ds_read_b128 v[228:231], v192 offset:37888
	ds_read_b128 v[244:247], v192 offset:38912
	ds_read_b128 v[248:251], v192 offset:39936
	s_waitcnt vmcnt(8)
	s_waitcnt lgkmcnt(0)
	s_barrier
	s_setprio 1
	s_waitcnt lgkmcnt(0)
	v_mfma_scale_f32_16x16x128_f8f6f4 v[150:153], v[10:17], v[206:213], v[150:153], v234, v235 op_sel_hi:[0,0,0]
	v_mfma_scale_f32_16x16x128_f8f6f4 v[146:149], v[26:33], v[206:213], v[146:149], v234, v235 op_sel_hi:[0,0,0]
	v_mfma_scale_f32_16x16x128_f8f6f4 v[142:145], v[10:17], v[216:223], v[142:145], v234, v235 op_sel_hi:[0,0,0]
	v_mfma_scale_f32_16x16x128_f8f6f4 v[138:141], v[26:33], v[216:223], v[138:141], v234, v235 op_sel_hi:[0,0,0]
	v_mfma_scale_f32_16x16x128_f8f6f4 v[134:137], v[10:17], v[224:231], v[134:137], v234, v235 op_sel_hi:[0,0,0]
	v_mfma_scale_f32_16x16x128_f8f6f4 v[130:133], v[26:33], v[224:231], v[130:133], v234, v235 op_sel_hi:[0,0,0]
	v_mfma_scale_f32_16x16x128_f8f6f4 v[126:129], v[10:17], v[244:251], v[126:129], v234, v235 op_sel_hi:[0,0,0]
	v_mfma_scale_f32_16x16x128_f8f6f4 v[122:125], v[26:33], v[244:251], v[122:125], v234, v235 op_sel_hi:[0,0,0]
	s_setprio 0
	s_setprio 1
	v_mfma_scale_f32_16x16x128_f8f6f4 v[118:121], v[2:9], v[206:213], v[118:121], v234, v235 op_sel_hi:[0,0,0]
	v_mfma_scale_f32_16x16x128_f8f6f4 v[114:117], v[198:205], v[206:213], v[114:117], v234, v235 op_sel_hi:[0,0,0]
	v_mfma_scale_f32_16x16x128_f8f6f4 v[110:113], v[2:9], v[216:223], v[110:113], v234, v235 op_sel_hi:[0,0,0]
	v_mfma_scale_f32_16x16x128_f8f6f4 v[106:109], v[198:205], v[216:223], v[106:109], v234, v235 op_sel_hi:[0,0,0]
	v_mfma_scale_f32_16x16x128_f8f6f4 v[102:105], v[2:9], v[224:231], v[102:105], v234, v235 op_sel_hi:[0,0,0]
	v_mfma_scale_f32_16x16x128_f8f6f4 v[98:101], v[198:205], v[224:231], v[98:101], v234, v235 op_sel_hi:[0,0,0]
	v_mfma_scale_f32_16x16x128_f8f6f4 v[94:97], v[2:9], v[244:251], v[94:97], v234, v235 op_sel_hi:[0,0,0]
	v_mfma_scale_f32_16x16x128_f8f6f4 v[90:93], v[198:205], v[244:251], v[90:93], v234, v235 op_sel_hi:[0,0,0]
	s_setprio 0
	s_nop 7
	s_mov_b32 m0, s64
	v_lshl_add_u64 v[18:19], v[18:19], 0, s[66:67]
	s_add_u32 s4, s56, 0x20080
	global_load_lds_dwordx4 v[18:19], off
	v_lshl_add_u64 v[18:19], v[20:21], 0, s[66:67]
	s_mov_b32 m0, s81
	s_addc_u32 s5, s57, 0
	global_load_lds_dwordx4 v[18:19], off
	v_lshl_add_u64 v[18:19], s[4:5], 0, v[162:163]
	s_mov_b32 m0, s49
	s_nop 0
	global_load_lds_dwordx4 v[18:19], off
	v_lshl_add_u64 v[18:19], s[4:5], 0, v[164:165]
	s_mov_b32 m0, s30
	s_nop 0
	global_load_lds_dwordx4 v[18:19], off
	v_lshl_add_u64 v[18:19], v[24:25], 0, s[66:67]
	s_mov_b32 m0, s6
	s_nop 0
	global_load_lds_dwordx4 v[18:19], off
	v_lshl_add_u64 v[18:19], v[22:23], 0, s[66:67]
	s_mov_b32 m0, s7
	s_nop 0
	global_load_lds_dwordx4 v[18:19], off
	s_barrier
	ds_read_b128 v[206:209], v192 offset:49152
	ds_read_b128 v[210:213], v192 offset:50176
	ds_read_b128 v[216:219], v192 offset:51200
	ds_read_b128 v[220:223], v192 offset:52224
	ds_read_b128 v[224:227], v192 offset:53248
	ds_read_b128 v[228:231], v192 offset:54272
	ds_read_b128 v[244:247], v192 offset:55296
	ds_read_b128 v[248:251], v192 offset:56320
	s_waitcnt vmcnt(8)
	s_waitcnt lgkmcnt(0)
	s_barrier
	s_setprio 1
	s_waitcnt lgkmcnt(0)
	v_mfma_scale_f32_16x16x128_f8f6f4 v[86:89], v[10:17], v[206:213], v[86:89], v234, v235 op_sel_hi:[0,0,0]
	v_mfma_scale_f32_16x16x128_f8f6f4 v[82:85], v[26:33], v[206:213], v[82:85], v234, v235 op_sel_hi:[0,0,0]
	v_mfma_scale_f32_16x16x128_f8f6f4 v[78:81], v[10:17], v[216:223], v[78:81], v234, v235 op_sel_hi:[0,0,0]
	v_mfma_scale_f32_16x16x128_f8f6f4 v[74:77], v[26:33], v[216:223], v[74:77], v234, v235 op_sel_hi:[0,0,0]
	v_mfma_scale_f32_16x16x128_f8f6f4 v[70:73], v[10:17], v[224:231], v[70:73], v234, v235 op_sel_hi:[0,0,0]
	v_mfma_scale_f32_16x16x128_f8f6f4 v[66:69], v[26:33], v[224:231], v[66:69], v234, v235 op_sel_hi:[0,0,0]
	v_mfma_scale_f32_16x16x128_f8f6f4 v[62:65], v[10:17], v[244:251], v[62:65], v234, v235 op_sel_hi:[0,0,0]
	v_mfma_scale_f32_16x16x128_f8f6f4 v[58:61], v[26:33], v[244:251], v[58:61], v234, v235 op_sel_hi:[0,0,0]
	s_setprio 0
	s_setprio 1
	v_mfma_scale_f32_16x16x128_f8f6f4 v[54:57], v[2:9], v[206:213], v[54:57], v234, v235 op_sel_hi:[0,0,0]
	v_mfma_scale_f32_16x16x128_f8f6f4 v[50:53], v[198:205], v[206:213], v[50:53], v234, v235 op_sel_hi:[0,0,0]
	v_mfma_scale_f32_16x16x128_f8f6f4 v[46:49], v[2:9], v[216:223], v[46:49], v234, v235 op_sel_hi:[0,0,0]
	v_mfma_scale_f32_16x16x128_f8f6f4 v[42:45], v[198:205], v[216:223], v[42:45], v234, v235 op_sel_hi:[0,0,0]
	v_mfma_scale_f32_16x16x128_f8f6f4 v[38:41], v[2:9], v[224:231], v[38:41], v234, v235 op_sel_hi:[0,0,0]
	v_mfma_scale_f32_16x16x128_f8f6f4 v[34:37], v[198:205], v[224:231], v[34:37], v234, v235 op_sel_hi:[0,0,0]
	v_mfma_scale_f32_16x16x128_f8f6f4 v[154:157], v[2:9], v[244:251], v[154:157], v234, v235 op_sel_hi:[0,0,0]
	v_mfma_scale_f32_16x16x128_f8f6f4 v[158:161], v[198:205], v[244:251], v[158:161], v234, v235 op_sel_hi:[0,0,0]
	s_setprio 0
	s_barrier
	s_add_i32 s74, s74, 2
	s_add_u32 s54, s54, 0x100
	s_addc_u32 s55, s55, 0
	s_add_u32 s43, s43, 0x100
	s_addc_u32 s45, s45, 0
	s_cmp_gt_u32 s74, 5
	s_cbranch_scc1 .LBB0_2005

.Lrw_done_g2_0:
	s_waitcnt lgkmcnt(0)
	s_barrier
	s_setprio 1
	s_waitcnt lgkmcnt(0)
	v_mfma_scale_f32_16x16x128_f8f6f4 v[158:161], v[18:25], v[172:179], 0, v234, v238 op_sel_hi:[0,0,0]
	v_mfma_scale_f32_16x16x128_f8f6f4 v[154:157], v[26:33], v[172:179], 0, v234, v238 op_sel_hi:[0,0,0]
	v_mfma_scale_f32_16x16x128_f8f6f4 v[150:153], v[18:25], v[198:205], 0, v234, v238 op_sel_hi:[0,0,0]
	v_mfma_scale_f32_16x16x128_f8f6f4 v[146:149], v[26:33], v[198:205], 0, v234, v238 op_sel_hi:[0,0,0]
	v_mfma_scale_f32_16x16x128_f8f6f4 v[142:145], v[18:25], v[206:213], 0, v234, v238 op_sel_hi:[0,0,0]
	v_mfma_scale_f32_16x16x128_f8f6f4 v[138:141], v[26:33], v[206:213], 0, v234, v238 op_sel_hi:[0,0,0]
	v_mfma_scale_f32_16x16x128_f8f6f4 v[134:137], v[18:25], v[216:223], 0, v234, v238 op_sel_hi:[0,0,0]
	v_mfma_scale_f32_16x16x128_f8f6f4 v[130:133], v[26:33], v[216:223], 0, v234, v238 op_sel_hi:[0,0,0]
	s_setprio 0
	s_setprio 1
	v_mfma_scale_f32_16x16x128_f8f6f4 v[126:129], v[2:9], v[172:179], 0, v234, v238 op_sel_hi:[0,0,0]
	v_mfma_scale_f32_16x16x128_f8f6f4 v[122:125], v[10:17], v[172:179], 0, v234, v238 op_sel_hi:[0,0,0]
	v_mfma_scale_f32_16x16x128_f8f6f4 v[118:121], v[2:9], v[198:205], 0, v234, v238 op_sel_hi:[0,0,0]
	v_mfma_scale_f32_16x16x128_f8f6f4 v[114:117], v[10:17], v[198:205], 0, v234, v238 op_sel_hi:[0,0,0]
	v_mfma_scale_f32_16x16x128_f8f6f4 v[110:113], v[2:9], v[206:213], 0, v234, v238 op_sel_hi:[0,0,0]
	v_mfma_scale_f32_16x16x128_f8f6f4 v[106:109], v[10:17], v[206:213], 0, v234, v238 op_sel_hi:[0,0,0]
	v_mfma_scale_f32_16x16x128_f8f6f4 v[102:105], v[2:9], v[216:223], 0, v234, v238 op_sel_hi:[0,0,0]
	v_mfma_scale_f32_16x16x128_f8f6f4 v[98:101], v[10:17], v[216:223], 0, v234, v238 op_sel_hi:[0,0,0]
	s_setprio 0
	s_nop 7
	v_lshl_add_u64 v[172:173], s[44:45], 0, v[0:1]
	s_mov_b64 s[48:49], 0x100
	s_mov_b32 m0, s41
	v_lshl_add_u64 v[174:175], v[172:173], 0, s[48:49]
	global_load_lds_dwordx4 v[174:175], off
	v_lshl_add_u64 v[174:175], s[44:45], 0, v[166:167]
	s_add_u32 s46, s44, 0x20100
	v_lshl_add_u64 v[176:177], v[174:175], 0, s[48:49]
	s_mov_b32 m0, s57
	s_addc_u32 s47, s45, 0
	global_load_lds_dwordx4 v[176:177], off
	v_lshl_add_u64 v[176:177], s[46:47], 0, v[0:1]
	s_mov_b32 m0, s58
	s_nop 0
	global_load_lds_dwordx4 v[176:177], off
	v_lshl_add_u64 v[176:177], s[46:47], 0, v[166:167]
	s_mov_b32 m0, s59
	s_nop 0
	global_load_lds_dwordx4 v[176:177], off
	v_lshl_add_u64 v[176:177], s[42:43], 0, v[162:163]
	v_lshl_add_u64 v[178:179], v[176:177], 0, s[48:49]
	s_mov_b32 m0, s37
	s_nop 0
	global_load_lds_dwordx4 v[178:179], off
	v_lshl_add_u64 v[178:179], s[42:43], 0, v[164:165]
	v_lshl_add_u64 v[232:233], v[178:179], 0, s[48:49]
	s_mov_b32 m0, s60
	s_nop 0
	global_load_lds_dwordx4 v[232:233], off
	s_barrier
	ds_read_b128 v[198:201], v196 offset:16384
	ds_read_b128 v[202:205], v196 offset:17408
	ds_read_b128 v[206:209], v196 offset:18432
	ds_read_b128 v[210:213], v196 offset:19456
	ds_read_b128 v[216:219], v196 offset:20480
	ds_read_b128 v[220:223], v196 offset:21504
	ds_read_b128 v[224:227], v196 offset:22528
	ds_read_b128 v[228:231], v196 offset:23552
	s_cmp_eq_u32 s26, 0
	s_cbranch_scc1 .Lrw_first_g2_1
	s_waitcnt vmcnt(24)
	s_branch .Lrw_done_g2_1

.Lrw_done_g2_1:
	s_waitcnt lgkmcnt(0)
	s_barrier
	s_setprio 1
	s_waitcnt lgkmcnt(0)
	v_mfma_scale_f32_16x16x128_f8f6f4 v[94:97], v[18:25], v[198:205], 0, v234, v238 op_sel_hi:[0,0,0]
	v_mfma_scale_f32_16x16x128_f8f6f4 v[90:93], v[26:33], v[198:205], 0, v234, v238 op_sel_hi:[0,0,0]
	v_mfma_scale_f32_16x16x128_f8f6f4 v[86:89], v[18:25], v[206:213], 0, v234, v238 op_sel_hi:[0,0,0]
	v_mfma_scale_f32_16x16x128_f8f6f4 v[82:85], v[26:33], v[206:213], 0, v234, v238 op_sel_hi:[0,0,0]
	v_mfma_scale_f32_16x16x128_f8f6f4 v[78:81], v[18:25], v[216:223], 0, v234, v238 op_sel_hi:[0,0,0]
	v_mfma_scale_f32_16x16x128_f8f6f4 v[74:77], v[26:33], v[216:223], 0, v234, v238 op_sel_hi:[0,0,0]
	v_mfma_scale_f32_16x16x128_f8f6f4 v[70:73], v[18:25], v[224:231], 0, v234, v238 op_sel_hi:[0,0,0]
	v_mfma_scale_f32_16x16x128_f8f6f4 v[66:69], v[26:33], v[224:231], 0, v234, v238 op_sel_hi:[0,0,0]
	s_setprio 0
	s_setprio 1
	v_mfma_scale_f32_16x16x128_f8f6f4 v[62:65], v[2:9], v[198:205], 0, v234, v238 op_sel_hi:[0,0,0]
	v_mfma_scale_f32_16x16x128_f8f6f4 v[58:61], v[10:17], v[198:205], 0, v234, v238 op_sel_hi:[0,0,0]
	v_mfma_scale_f32_16x16x128_f8f6f4 v[54:57], v[2:9], v[206:213], 0, v234, v238 op_sel_hi:[0,0,0]
	v_mfma_scale_f32_16x16x128_f8f6f4 v[50:53], v[10:17], v[206:213], 0, v234, v238 op_sel_hi:[0,0,0]
	v_mfma_scale_f32_16x16x128_f8f6f4 v[46:49], v[2:9], v[216:223], 0, v234, v238 op_sel_hi:[0,0,0]
	v_mfma_scale_f32_16x16x128_f8f6f4 v[42:45], v[10:17], v[216:223], 0, v234, v238 op_sel_hi:[0,0,0]
	v_mfma_scale_f32_16x16x128_f8f6f4 v[38:41], v[2:9], v[224:231], 0, v234, v238 op_sel_hi:[0,0,0]
	v_mfma_scale_f32_16x16x128_f8f6f4 v[34:37], v[10:17], v[224:231], 0, v234, v238 op_sel_hi:[0,0,0]
	s_setprio 0
	s_nop 7
	s_add_u32 s46, s42, 0x20100
	s_addc_u32 s47, s43, 0
	s_mov_b32 m0, s61
	v_lshl_add_u64 v[232:233], s[46:47], 0, v[162:163]
	global_load_lds_dwordx4 v[232:233], off
	v_lshl_add_u64 v[232:233], s[46:47], 0, v[164:165]
	s_mov_b32 m0, s62
	s_nop 0
	global_load_lds_dwordx4 v[232:233], off
	s_barrier
	ds_read_b128 v[18:21], v188
	ds_read_b128 v[22:25], v189
	ds_read_b128 v[26:29], v190
	ds_read_b128 v[30:33], v191
	ds_read_b128 v[2:5], v192
	ds_read_b128 v[6:9], v193
	ds_read_b128 v[10:13], v194
	ds_read_b128 v[14:17], v195
	ds_read_b128 v[198:201], v196 offset:32768
	ds_read_b128 v[202:205], v196 offset:33792
	ds_read_b128 v[206:209], v196 offset:34816
	ds_read_b128 v[210:213], v196 offset:35840
	ds_read_b128 v[216:219], v196 offset:36864
	ds_read_b128 v[220:223], v196 offset:37888
	ds_read_b128 v[224:227], v196 offset:38912
	ds_read_b128 v[228:231], v196 offset:39936
	s_waitcnt vmcnt(8)
	s_waitcnt lgkmcnt(0)
	s_barrier
	s_setprio 1
	s_waitcnt lgkmcnt(0)
	v_mfma_scale_f32_16x16x128_f8f6f4 v[158:161], v[18:25], v[198:205], v[158:161], v234, v238 op_sel_hi:[0,0,0]
	v_mfma_scale_f32_16x16x128_f8f6f4 v[154:157], v[26:33], v[198:205], v[154:157], v234, v238 op_sel_hi:[0,0,0]
	v_mfma_scale_f32_16x16x128_f8f6f4 v[150:153], v[18:25], v[206:213], v[150:153], v234, v238 op_sel_hi:[0,0,0]
	v_mfma_scale_f32_16x16x128_f8f6f4 v[146:149], v[26:33], v[206:213], v[146:149], v234, v238 op_sel_hi:[0,0,0]
	v_mfma_scale_f32_16x16x128_f8f6f4 v[142:145], v[18:25], v[216:223], v[142:145], v234, v238 op_sel_hi:[0,0,0]
	v_mfma_scale_f32_16x16x128_f8f6f4 v[138:141], v[26:33], v[216:223], v[138:141], v234, v238 op_sel_hi:[0,0,0]
	v_mfma_scale_f32_16x16x128_f8f6f4 v[134:137], v[18:25], v[224:231], v[134:137], v234, v238 op_sel_hi:[0,0,0]
	v_mfma_scale_f32_16x16x128_f8f6f4 v[130:133], v[26:33], v[224:231], v[130:133], v234, v238 op_sel_hi:[0,0,0]
	s_setprio 0
	s_setprio 1
	v_mfma_scale_f32_16x16x128_f8f6f4 v[126:129], v[2:9], v[198:205], v[126:129], v234, v238 op_sel_hi:[0,0,0]
	v_mfma_scale_f32_16x16x128_f8f6f4 v[122:125], v[10:17], v[198:205], v[122:125], v234, v238 op_sel_hi:[0,0,0]
	v_mfma_scale_f32_16x16x128_f8f6f4 v[118:121], v[2:9], v[206:213], v[118:121], v234, v238 op_sel_hi:[0,0,0]
	v_mfma_scale_f32_16x16x128_f8f6f4 v[114:117], v[10:17], v[206:213], v[114:117], v234, v238 op_sel_hi:[0,0,0]
	v_mfma_scale_f32_16x16x128_f8f6f4 v[110:113], v[2:9], v[216:223], v[110:113], v234, v238 op_sel_hi:[0,0,0]
	v_mfma_scale_f32_16x16x128_f8f6f4 v[106:109], v[10:17], v[216:223], v[106:109], v234, v238 op_sel_hi:[0,0,0]
	v_mfma_scale_f32_16x16x128_f8f6f4 v[102:105], v[2:9], v[224:231], v[102:105], v234, v238 op_sel_hi:[0,0,0]
	v_mfma_scale_f32_16x16x128_f8f6f4 v[98:101], v[10:17], v[224:231], v[98:101], v234, v238 op_sel_hi:[0,0,0]
	s_setprio 0
	s_nop 7
	s_mov_b64 s[48:49], 0x180
	s_mov_b32 m0, s65
	v_lshl_add_u64 v[172:173], v[172:173], 0, s[48:49]
	s_add_u32 s46, s44, 0x20180
	global_load_lds_dwordx4 v[172:173], off
	v_lshl_add_u64 v[172:173], v[174:175], 0, s[48:49]
	s_mov_b32 m0, s68
	s_addc_u32 s47, s45, 0
	global_load_lds_dwordx4 v[172:173], off
	v_lshl_add_u64 v[172:173], s[46:47], 0, v[0:1]
	s_mov_b32 m0, s51
	s_nop 0
	global_load_lds_dwordx4 v[172:173], off
	v_lshl_add_u64 v[172:173], s[46:47], 0, v[166:167]
	s_mov_b32 m0, s4
	s_nop 0
	global_load_lds_dwordx4 v[172:173], off
	v_lshl_add_u64 v[172:173], v[176:177], 0, s[48:49]
	s_mov_b32 m0, s81
	s_nop 0
	global_load_lds_dwordx4 v[172:173], off
	v_lshl_add_u64 v[172:173], v[178:179], 0, s[48:49]
	s_mov_b32 m0, s50
	s_nop 0
	global_load_lds_dwordx4 v[172:173], off
	s_barrier
	ds_read_b128 v[198:201], v196 offset:49152
	ds_read_b128 v[202:205], v196 offset:50176
	ds_read_b128 v[206:209], v196 offset:51200
	ds_read_b128 v[210:213], v196 offset:52224
	ds_read_b128 v[216:219], v196 offset:53248
	ds_read_b128 v[220:223], v196 offset:54272
	ds_read_b128 v[224:227], v196 offset:55296
	ds_read_b128 v[228:231], v196 offset:56320
	s_waitcnt vmcnt(8)
	s_waitcnt lgkmcnt(0)
	s_barrier
	s_setprio 1
	s_waitcnt lgkmcnt(0)
	v_mfma_scale_f32_16x16x128_f8f6f4 v[94:97], v[18:25], v[198:205], v[94:97], v234, v238 op_sel_hi:[0,0,0]
	v_mfma_scale_f32_16x16x128_f8f6f4 v[90:93], v[26:33], v[198:205], v[90:93], v234, v238 op_sel_hi:[0,0,0]
	v_mfma_scale_f32_16x16x128_f8f6f4 v[86:89], v[18:25], v[206:213], v[86:89], v234, v238 op_sel_hi:[0,0,0]
	v_mfma_scale_f32_16x16x128_f8f6f4 v[82:85], v[26:33], v[206:213], v[82:85], v234, v238 op_sel_hi:[0,0,0]
	v_mfma_scale_f32_16x16x128_f8f6f4 v[78:81], v[18:25], v[216:223], v[78:81], v234, v238 op_sel_hi:[0,0,0]
	v_mfma_scale_f32_16x16x128_f8f6f4 v[74:77], v[26:33], v[216:223], v[74:77], v234, v238 op_sel_hi:[0,0,0]
	v_mfma_scale_f32_16x16x128_f8f6f4 v[70:73], v[18:25], v[224:231], v[70:73], v234, v238 op_sel_hi:[0,0,0]
	v_mfma_scale_f32_16x16x128_f8f6f4 v[66:69], v[26:33], v[224:231], v[66:69], v234, v238 op_sel_hi:[0,0,0]
	s_setprio 0
	s_setprio 1
	v_mfma_scale_f32_16x16x128_f8f6f4 v[62:65], v[2:9], v[198:205], v[62:65], v234, v238 op_sel_hi:[0,0,0]
	v_mfma_scale_f32_16x16x128_f8f6f4 v[58:61], v[10:17], v[198:205], v[58:61], v234, v238 op_sel_hi:[0,0,0]
	v_mfma_scale_f32_16x16x128_f8f6f4 v[54:57], v[2:9], v[206:213], v[54:57], v234, v238 op_sel_hi:[0,0,0]
	v_mfma_scale_f32_16x16x128_f8f6f4 v[50:53], v[10:17], v[206:213], v[50:53], v234, v238 op_sel_hi:[0,0,0]
	v_mfma_scale_f32_16x16x128_f8f6f4 v[46:49], v[2:9], v[216:223], v[46:49], v234, v238 op_sel_hi:[0,0,0]
	v_mfma_scale_f32_16x16x128_f8f6f4 v[42:45], v[10:17], v[216:223], v[42:45], v234, v238 op_sel_hi:[0,0,0]
	v_mfma_scale_f32_16x16x128_f8f6f4 v[38:41], v[2:9], v[224:231], v[38:41], v234, v238 op_sel_hi:[0,0,0]
	v_mfma_scale_f32_16x16x128_f8f6f4 v[34:37], v[10:17], v[224:231], v[34:37], v234, v238 op_sel_hi:[0,0,0]
	s_setprio 0
	s_barrier
	s_add_u32 s42, s42, 0x20180
	s_addc_u32 s43, s43, 0
	s_add_u32 s48, s44, 0x200
	s_addc_u32 s49, s45, 0
	s_mov_b32 s74, 0
.LBB0_2089:
	ds_read_b128 v[2:5], v180
	ds_read_b128 v[6:9], v181
	ds_read_b128 v[10:13], v182
	ds_read_b128 v[14:17], v183
	ds_read_b128 v[26:29], v184
	ds_read_b128 v[30:33], v185
	ds_read_b128 v[172:175], v186
	ds_read_b128 v[176:179], v187
	s_add_u32 s44, s42, 0xfffe0080
	s_addc_u32 s45, s43, -1
	s_cmp_eq_u32 s74, 4
	s_cselect_b32 s47, s13, s45
	s_cselect_b32 s46, s27, s44
	s_cselect_b32 s45, s35, s49
	s_cselect_b32 s44, s34, s48
	s_mov_b32 m0, s29
	v_lshl_add_u64 v[224:225], s[42:43], 0, v[168:169]
	ds_read_b128 v[18:21], v196
	ds_read_b128 v[22:25], v196 offset:1024
	ds_read_b128 v[198:201], v196 offset:2048
	ds_read_b128 v[202:205], v196 offset:3072
	ds_read_b128 v[206:209], v196 offset:4096
	ds_read_b128 v[210:213], v196 offset:5120
	ds_read_b128 v[216:219], v196 offset:6144
	ds_read_b128 v[220:223], v196 offset:7168
	global_load_lds_dwordx4 v[224:225], off
	v_lshl_add_u64 v[224:225], s[42:43], 0, v[170:171]
	s_mov_b32 m0, s31
	s_nop 0
	global_load_lds_dwordx4 v[224:225], off
	s_waitcnt vmcnt(8)
	s_waitcnt lgkmcnt(0)
	s_barrier
	s_setprio 1
	s_waitcnt lgkmcnt(0)
	v_mfma_scale_f32_16x16x128_f8f6f4 v[158:161], v[2:9], v[18:25], v[158:161], v234, v238 op_sel_hi:[0,0,0]
	v_mfma_scale_f32_16x16x128_f8f6f4 v[154:157], v[10:17], v[18:25], v[154:157], v234, v238 op_sel_hi:[0,0,0]
	v_mfma_scale_f32_16x16x128_f8f6f4 v[150:153], v[2:9], v[198:205], v[150:153], v234, v238 op_sel_hi:[0,0,0]
	v_mfma_scale_f32_16x16x128_f8f6f4 v[146:149], v[10:17], v[198:205], v[146:149], v234, v238 op_sel_hi:[0,0,0]
	v_mfma_scale_f32_16x16x128_f8f6f4 v[142:145], v[2:9], v[206:213], v[142:145], v234, v238 op_sel_hi:[0,0,0]
	v_mfma_scale_f32_16x16x128_f8f6f4 v[138:141], v[10:17], v[206:213], v[138:141], v234, v238 op_sel_hi:[0,0,0]
	v_mfma_scale_f32_16x16x128_f8f6f4 v[134:137], v[2:9], v[216:223], v[134:137], v234, v238 op_sel_hi:[0,0,0]
	v_mfma_scale_f32_16x16x128_f8f6f4 v[130:133], v[10:17], v[216:223], v[130:133], v234, v238 op_sel_hi:[0,0,0]
	s_setprio 0
	s_setprio 1
	v_mfma_scale_f32_16x16x128_f8f6f4 v[126:129], v[26:33], v[18:25], v[126:129], v234, v238 op_sel_hi:[0,0,0]
	v_mfma_scale_f32_16x16x128_f8f6f4 v[122:125], v[172:179], v[18:25], v[122:125], v234, v238 op_sel_hi:[0,0,0]
	v_mfma_scale_f32_16x16x128_f8f6f4 v[118:121], v[26:33], v[198:205], v[118:121], v234, v238 op_sel_hi:[0,0,0]
	v_mfma_scale_f32_16x16x128_f8f6f4 v[114:117], v[172:179], v[198:205], v[114:117], v234, v238 op_sel_hi:[0,0,0]
	v_mfma_scale_f32_16x16x128_f8f6f4 v[110:113], v[26:33], v[206:213], v[110:113], v234, v238 op_sel_hi:[0,0,0]
	v_mfma_scale_f32_16x16x128_f8f6f4 v[106:109], v[172:179], v[206:213], v[106:109], v234, v238 op_sel_hi:[0,0,0]
	v_mfma_scale_f32_16x16x128_f8f6f4 v[102:105], v[26:33], v[216:223], v[102:105], v234, v238 op_sel_hi:[0,0,0]
	v_mfma_scale_f32_16x16x128_f8f6f4 v[98:101], v[172:179], v[216:223], v[98:101], v234, v238 op_sel_hi:[0,0,0]
	s_setprio 0
	s_nop 7
	s_mov_b32 m0, s41
	v_lshl_add_u64 v[18:19], s[44:45], 0, v[0:1]
	s_add_u32 vcc_lo, s44, 0x20000
	global_load_lds_dwordx4 v[18:19], off
	v_lshl_add_u64 v[20:21], s[44:45], 0, v[166:167]
	s_mov_b32 m0, s57
	s_addc_u32 vcc_hi, s45, 0
	global_load_lds_dwordx4 v[20:21], off
	v_lshl_add_u64 v[22:23], vcc, 0, v[0:1]
	s_mov_b32 m0, s58
	v_lshl_add_u64 v[24:25], s[46:47], 0, v[164:165]
	global_load_lds_dwordx4 v[22:23], off
	v_lshl_add_u64 v[22:23], vcc, 0, v[166:167]
	s_mov_b32 m0, s59
	s_nop 0
	global_load_lds_dwordx4 v[22:23], off
	v_lshl_add_u64 v[22:23], s[46:47], 0, v[162:163]
	s_mov_b32 m0, s37
	s_nop 0
	global_load_lds_dwordx4 v[22:23], off
	s_mov_b32 m0, s60
	s_nop 0
	global_load_lds_dwordx4 v[24:25], off
	s_barrier
	ds_read_b128 v[198:201], v196 offset:16384
	ds_read_b128 v[202:205], v196 offset:17408
	ds_read_b128 v[206:209], v196 offset:18432
	ds_read_b128 v[210:213], v196 offset:19456
	ds_read_b128 v[216:219], v196 offset:20480
	ds_read_b128 v[220:223], v196 offset:21504
	ds_read_b128 v[224:227], v196 offset:22528
	ds_read_b128 v[228:231], v196 offset:23552
	s_waitcnt vmcnt(8)
	s_waitcnt lgkmcnt(0)
	s_barrier
	s_setprio 1
	s_waitcnt lgkmcnt(0)
	v_mfma_scale_f32_16x16x128_f8f6f4 v[94:97], v[2:9], v[198:205], v[94:97], v234, v238 op_sel_hi:[0,0,0]
	v_mfma_scale_f32_16x16x128_f8f6f4 v[90:93], v[10:17], v[198:205], v[90:93], v234, v238 op_sel_hi:[0,0,0]
	v_mfma_scale_f32_16x16x128_f8f6f4 v[86:89], v[2:9], v[206:213], v[86:89], v234, v238 op_sel_hi:[0,0,0]
	v_mfma_scale_f32_16x16x128_f8f6f4 v[82:85], v[10:17], v[206:213], v[82:85], v234, v238 op_sel_hi:[0,0,0]
	v_mfma_scale_f32_16x16x128_f8f6f4 v[78:81], v[2:9], v[216:223], v[78:81], v234, v238 op_sel_hi:[0,0,0]
	v_mfma_scale_f32_16x16x128_f8f6f4 v[74:77], v[10:17], v[216:223], v[74:77], v234, v238 op_sel_hi:[0,0,0]
	v_mfma_scale_f32_16x16x128_f8f6f4 v[70:73], v[2:9], v[224:231], v[70:73], v234, v238 op_sel_hi:[0,0,0]
	v_mfma_scale_f32_16x16x128_f8f6f4 v[66:69], v[10:17], v[224:231], v[66:69], v234, v238 op_sel_hi:[0,0,0]
	s_setprio 0
	s_setprio 1
	v_mfma_scale_f32_16x16x128_f8f6f4 v[62:65], v[26:33], v[198:205], v[62:65], v234, v238 op_sel_hi:[0,0,0]
	v_mfma_scale_f32_16x16x128_f8f6f4 v[58:61], v[172:179], v[198:205], v[58:61], v234, v238 op_sel_hi:[0,0,0]
	v_mfma_scale_f32_16x16x128_f8f6f4 v[54:57], v[26:33], v[206:213], v[54:57], v234, v238 op_sel_hi:[0,0,0]
	v_mfma_scale_f32_16x16x128_f8f6f4 v[50:53], v[172:179], v[206:213], v[50:53], v234, v238 op_sel_hi:[0,0,0]
	v_mfma_scale_f32_16x16x128_f8f6f4 v[46:49], v[26:33], v[216:223], v[46:49], v234, v238 op_sel_hi:[0,0,0]
	v_mfma_scale_f32_16x16x128_f8f6f4 v[42:45], v[172:179], v[216:223], v[42:45], v234, v238 op_sel_hi:[0,0,0]
	v_mfma_scale_f32_16x16x128_f8f6f4 v[38:41], v[26:33], v[224:231], v[38:41], v234, v238 op_sel_hi:[0,0,0]
	v_mfma_scale_f32_16x16x128_f8f6f4 v[34:37], v[172:179], v[224:231], v[34:37], v234, v238 op_sel_hi:[0,0,0]
	s_setprio 0
	s_nop 7
	s_add_u32 s46, s46, 0x20000
	s_addc_u32 s47, s47, 0
	s_mov_b32 m0, s61
	v_lshl_add_u64 v[232:233], s[46:47], 0, v[162:163]
	global_load_lds_dwordx4 v[232:233], off
	v_lshl_add_u64 v[232:233], s[46:47], 0, v[164:165]
	s_mov_b32 m0, s62
	s_nop 0
	global_load_lds_dwordx4 v[232:233], off
	s_barrier
	ds_read_b128 v[10:13], v188
	ds_read_b128 v[14:17], v189
	ds_read_b128 v[26:29], v190
	ds_read_b128 v[30:33], v191
	ds_read_b128 v[2:5], v192
	ds_read_b128 v[6:9], v193
	ds_read_b128 v[172:175], v194
	ds_read_b128 v[176:179], v195
	ds_read_b128 v[198:201], v196 offset:32768
	ds_read_b128 v[202:205], v196 offset:33792
	ds_read_b128 v[206:209], v196 offset:34816
	ds_read_b128 v[210:213], v196 offset:35840
	ds_read_b128 v[216:219], v196 offset:36864
	ds_read_b128 v[220:223], v196 offset:37888
	ds_read_b128 v[224:227], v196 offset:38912
	ds_read_b128 v[228:231], v196 offset:39936
	s_waitcnt vmcnt(8)
	s_waitcnt lgkmcnt(0)
	s_barrier
	s_setprio 1
	s_waitcnt lgkmcnt(0)
	v_mfma_scale_f32_16x16x128_f8f6f4 v[158:161], v[10:17], v[198:205], v[158:161], v234, v238 op_sel_hi:[0,0,0]
	v_mfma_scale_f32_16x16x128_f8f6f4 v[154:157], v[26:33], v[198:205], v[154:157], v234, v238 op_sel_hi:[0,0,0]
	v_mfma_scale_f32_16x16x128_f8f6f4 v[150:153], v[10:17], v[206:213], v[150:153], v234, v238 op_sel_hi:[0,0,0]
	v_mfma_scale_f32_16x16x128_f8f6f4 v[146:149], v[26:33], v[206:213], v[146:149], v234, v238 op_sel_hi:[0,0,0]
	v_mfma_scale_f32_16x16x128_f8f6f4 v[142:145], v[10:17], v[216:223], v[142:145], v234, v238 op_sel_hi:[0,0,0]
	v_mfma_scale_f32_16x16x128_f8f6f4 v[138:141], v[26:33], v[216:223], v[138:141], v234, v238 op_sel_hi:[0,0,0]
	v_mfma_scale_f32_16x16x128_f8f6f4 v[134:137], v[10:17], v[224:231], v[134:137], v234, v238 op_sel_hi:[0,0,0]
	v_mfma_scale_f32_16x16x128_f8f6f4 v[130:133], v[26:33], v[224:231], v[130:133], v234, v238 op_sel_hi:[0,0,0]
	s_setprio 0
	s_setprio 1
	v_mfma_scale_f32_16x16x128_f8f6f4 v[126:129], v[2:9], v[198:205], v[126:129], v234, v238 op_sel_hi:[0,0,0]
	v_mfma_scale_f32_16x16x128_f8f6f4 v[122:125], v[172:179], v[198:205], v[122:125], v234, v238 op_sel_hi:[0,0,0]
	v_mfma_scale_f32_16x16x128_f8f6f4 v[118:121], v[2:9], v[206:213], v[118:121], v234, v238 op_sel_hi:[0,0,0]
	v_mfma_scale_f32_16x16x128_f8f6f4 v[114:117], v[172:179], v[206:213], v[114:117], v234, v238 op_sel_hi:[0,0,0]
	v_mfma_scale_f32_16x16x128_f8f6f4 v[110:113], v[2:9], v[216:223], v[110:113], v234, v238 op_sel_hi:[0,0,0]
	v_mfma_scale_f32_16x16x128_f8f6f4 v[106:109], v[172:179], v[216:223], v[106:109], v234, v238 op_sel_hi:[0,0,0]
	v_mfma_scale_f32_16x16x128_f8f6f4 v[102:105], v[2:9], v[224:231], v[102:105], v234, v238 op_sel_hi:[0,0,0]
	v_mfma_scale_f32_16x16x128_f8f6f4 v[98:101], v[172:179], v[224:231], v[98:101], v234, v238 op_sel_hi:[0,0,0]
	s_setprio 0
	s_nop 7
	s_mov_b32 m0, s65
	v_lshl_add_u64 v[18:19], v[18:19], 0, s[66:67]
	s_add_u32 s44, s44, 0x20080
	global_load_lds_dwordx4 v[18:19], off
	v_lshl_add_u64 v[18:19], v[20:21], 0, s[66:67]
	s_mov_b32 m0, s68
	s_addc_u32 s45, s45, 0
	global_load_lds_dwordx4 v[18:19], off
	v_lshl_add_u64 v[18:19], s[44:45], 0, v[0:1]
	s_mov_b32 m0, s51
	s_nop 0
	global_load_lds_dwordx4 v[18:19], off
	v_lshl_add_u64 v[18:19], s[44:45], 0, v[166:167]
	s_mov_b32 m0, s4
	s_nop 0
	global_load_lds_dwordx4 v[18:19], off
	v_lshl_add_u64 v[18:19], v[22:23], 0, s[66:67]
	s_mov_b32 m0, s81
	s_nop 0
	global_load_lds_dwordx4 v[18:19], off
	v_lshl_add_u64 v[18:19], v[24:25], 0, s[66:67]
	s_mov_b32 m0, s50
	s_nop 0
	global_load_lds_dwordx4 v[18:19], off
	s_barrier
	ds_read_b128 v[198:201], v196 offset:49152
	ds_read_b128 v[202:205], v196 offset:50176
	ds_read_b128 v[206:209], v196 offset:51200
	ds_read_b128 v[210:213], v196 offset:52224
	ds_read_b128 v[216:219], v196 offset:53248
	ds_read_b128 v[220:223], v196 offset:54272
	ds_read_b128 v[224:227], v196 offset:55296
	ds_read_b128 v[228:231], v196 offset:56320
	s_waitcnt vmcnt(8)
	s_waitcnt lgkmcnt(0)
	s_barrier
	s_setprio 1
	s_waitcnt lgkmcnt(0)
	v_mfma_scale_f32_16x16x128_f8f6f4 v[94:97], v[10:17], v[198:205], v[94:97], v234, v238 op_sel_hi:[0,0,0]
	v_mfma_scale_f32_16x16x128_f8f6f4 v[90:93], v[26:33], v[198:205], v[90:93], v234, v238 op_sel_hi:[0,0,0]
	v_mfma_scale_f32_16x16x128_f8f6f4 v[86:89], v[10:17], v[206:213], v[86:89], v234, v238 op_sel_hi:[0,0,0]
	v_mfma_scale_f32_16x16x128_f8f6f4 v[82:85], v[26:33], v[206:213], v[82:85], v234, v238 op_sel_hi:[0,0,0]
	v_mfma_scale_f32_16x16x128_f8f6f4 v[78:81], v[10:17], v[216:223], v[78:81], v234, v238 op_sel_hi:[0,0,0]
	v_mfma_scale_f32_16x16x128_f8f6f4 v[74:77], v[26:33], v[216:223], v[74:77], v234, v238 op_sel_hi:[0,0,0]
	v_mfma_scale_f32_16x16x128_f8f6f4 v[70:73], v[10:17], v[224:231], v[70:73], v234, v238 op_sel_hi:[0,0,0]
	v_mfma_scale_f32_16x16x128_f8f6f4 v[66:69], v[26:33], v[224:231], v[66:69], v234, v238 op_sel_hi:[0,0,0]
	s_setprio 0
	s_setprio 1
	v_mfma_scale_f32_16x16x128_f8f6f4 v[62:65], v[2:9], v[198:205], v[62:65], v234, v238 op_sel_hi:[0,0,0]
	v_mfma_scale_f32_16x16x128_f8f6f4 v[58:61], v[172:179], v[198:205], v[58:61], v234, v238 op_sel_hi:[0,0,0]
	v_mfma_scale_f32_16x16x128_f8f6f4 v[54:57], v[2:9], v[206:213], v[54:57], v234, v238 op_sel_hi:[0,0,0]
	v_mfma_scale_f32_16x16x128_f8f6f4 v[50:53], v[172:179], v[206:213], v[50:53], v234, v238 op_sel_hi:[0,0,0]
	v_mfma_scale_f32_16x16x128_f8f6f4 v[46:49], v[2:9], v[216:223], v[46:49], v234, v238 op_sel_hi:[0,0,0]
	v_mfma_scale_f32_16x16x128_f8f6f4 v[42:45], v[172:179], v[216:223], v[42:45], v234, v238 op_sel_hi:[0,0,0]
	v_mfma_scale_f32_16x16x128_f8f6f4 v[38:41], v[2:9], v[224:231], v[38:41], v234, v238 op_sel_hi:[0,0,0]
	v_mfma_scale_f32_16x16x128_f8f6f4 v[34:37], v[172:179], v[224:231], v[34:37], v234, v238 op_sel_hi:[0,0,0]
	s_setprio 0
	s_barrier
	s_add_i32 s74, s74, 2
	s_add_u32 s42, s42, 0x100
	s_addc_u32 s43, s43, 0
	s_add_u32 s48, s48, 0x100
	s_addc_u32 s49, s49, 0
	s_cmp_gt_u32 s74, 5
	s_cbranch_scc0 .LBB0_2089
	s_branch .Lg2_join
